# speedup vs baseline: 1.0412x; 1.0080x over previous
.Lmy_loopb:
	ds_read_b128 v[158:161], v248 offset:0
	ds_read_b128 v[162:165], v248 offset:1024
	ds_read_b128 v[166:169], v249 offset:2048
	ds_read_b128 v[170:173], v249 offset:3072
	v_mfma_f32_16x16x32_f16 v[218:221], v[82:85], v[150:153], v[106:109]
	v_mfma_f32_16x16x32_f16 v[222:225], v[90:93], v[150:153], v[110:113]
	v_mfma_f32_16x16x32_f16 v[218:221], v[86:89], v[154:157], v[218:221]
	v_mfma_f32_16x16x32_f16 v[222:225], v[94:97], v[154:157], v[222:225]
	s_waitcnt lgkmcnt(2)
	v_mfma_f32_16x16x32_f16 v[210:213], v[54:57], v[158:161], v[210:213]
	v_mfma_f32_16x16x32_f16 v[210:213], v[58:61], v[162:165], v[210:213]
	s_waitcnt lgkmcnt(0)
	v_mfma_f32_16x16x32_f16 v[210:213], v[62:65], v[166:169], v[210:213]
	v_mfma_f32_16x16x32_f16 v[210:213], v[50:53], v[170:173], v[210:213]
	s_waitcnt vmcnt(9)
	v_cvt_pk_f16_f32 v251, v192, v193
	ds_write_b32 v1, v251 offset:0
	ds_read_b128 v[150:153], v186 offset:6144
	ds_read_b128 v[154:157], v186 offset:7168
	s_nop 2
	v_exp_f32_e32 v226, v210
	v_exp_f32_e32 v227, v211
	v_mfma_f32_16x16x32_f16 v[214:217], v[34:37], v[158:161], v[214:217]
	v_min_f32_e32 v228, s42, v212
	v_exp_f32_e32 v229, v213
	v_mfma_f32_16x16x32_f16 v[214:217], v[38:41], v[162:165], v[214:217]
	v_exp_f32_e32 v228, v228
	v_add_f32_e32 v227, 1.0, v227
	v_mfma_f32_16x16x32_f16 v[214:217], v[42:45], v[166:169], v[214:217]
	v_fma_f32 v230, v228, s41, s41
	v_rcp_f32_e32 v227, v227
	v_mfma_f32_16x16x32_f16 v[214:217], v[46:49], v[170:173], v[214:217]
	v_fma_f32 v230, v226, v230, v230
	v_rcp_f32_e32 v230, v230
	v_mfma_f32_16x16x32_f16 v[218:221], v[18:21], v[158:161], v[218:221]
	v_fma_f32 v226, -v228, v230, v230
	v_fma_f32 v200, v200, v227, v226
	v_mfma_f32_16x16x32_f16 v[218:221], v[14:17], v[162:165], v[218:221]
	v_exp_f32_e32 v226, v200
	s_nop 0
	v_add_f32_e32 v227, 1.0, v226
	v_mfma_f32_16x16x32_f16 v[218:221], v[10:13], v[166:169], v[218:221]
	v_fma_f32 v227, v229, v227, v227
	v_rcp_f32_e32 v227, v227
	v_mfma_f32_16x16x32_f16 v[218:221], v[26:29], v[170:173], v[218:221]
	v_fma_f32 v226, -v226, v227, v227
	v_exp_f32_e32 v231, v214
	v_mfma_f32_16x16x32_f16 v[222:225], v[2:5], v[158:161], v[222:225]
	v_exp_f32_e32 v232, v215
	v_min_f32_e32 v233, s42, v216
	v_mfma_f32_16x16x32_f16 v[222:225], v[6:9], v[162:165], v[222:225]
	v_exp_f32_e32 v234, v217
	v_exp_f32_e32 v233, v233
	v_mfma_f32_16x16x32_f16 v[222:225], v[22:25], v[166:169], v[222:225]
	v_exp_f32_e32 v236, v218
	v_add_f32_e32 v232, 1.0, v232
	v_mfma_f32_16x16x32_f16 v[222:225], v[30:33], v[170:173], v[222:225]
	v_fma_f32 v235, v233, s41, s41
	v_exp_f32_e32 v227, v219
	v_rcp_f32_e32 v232, v232
	v_fma_f32 v235, v231, v235, v235
	v_min_f32_e32 v228, s42, v220
	v_rcp_f32_e32 v235, v235
	s_nop 0
	v_fma_f32 v231, -v233, v235, v235
	v_exp_f32_e32 v229, v221
	v_fma_f32 v201, v201, v232, v231
	v_exp_f32_e32 v231, v201
	v_exp_f32_e32 v228, v228
	v_add_f32_e32 v232, 1.0, v231
	v_fma_f32 v232, v234, v232, v232
	v_add_f32_e32 v227, 1.0, v227
	v_rcp_f32_e32 v232, v232
	v_mfma_f32_16x16x32_f16 v[146:149], v[122:125], v[158:161], v[146:149]
	v_fma_f32 v231, -v231, v232, v232
	v_fma_f32 v230, v228, s41, s41
	v_cvt_pk_f16_f32 v246, v226, v231
	v_mfma_f32_16x16x32_f16 v[146:149], v[126:129], v[162:165], v[146:149]
	v_exp_f32_e32 v231, v222
	v_rcp_f32_e32 v227, v227
	v_exp_f32_e32 v232, v223
	buffer_load_dwordx4 v[122:125], v189, s[76:79], s46 offen
	buffer_load_dwordx4 v[126:129], v208, s[76:79], s46 offen
	v_min_f32_e32 v233, s42, v224
	v_fma_f32 v230, v236, v230, v230
	v_exp_f32_e32 v234, v225
	s_waitcnt lgkmcnt(0)
	v_mfma_f32_16x16x32_f16 v[210:213], v[70:73], v[150:153], v[98:101]
	v_exp_f32_e32 v233, v233
	v_rcp_f32_e32 v230, v230
	v_add_f32_e32 v232, 1.0, v232
	v_mfma_f32_16x16x32_f16 v[214:217], v[74:77], v[150:153], v[102:105]
	v_fma_f32 v235, v233, s41, s41
	v_fma_f32 v236, -v228, v230, v230
	v_rcp_f32_e32 v232, v232
	v_fma_f32 v235, v231, v235, v235
	v_fma_f32 v198, v198, v227, v236
	v_rcp_f32_e32 v235, v235
	s_nop 0
	v_fma_f32 v231, -v233, v235, v235
	v_exp_f32_e32 v236, v198
	v_fma_f32 v199, v199, v232, v231
	v_exp_f32_e32 v231, v199
	v_add_f32_e32 v227, 1.0, v236
	v_add_f32_e32 v232, 1.0, v231
	v_fma_f32 v232, v234, v232, v232
	v_fma_f32 v227, v229, v227, v227
	v_rcp_f32_e32 v232, v232
	s_nop 0
	v_fma_f32 v231, -v231, v232, v232
	v_rcp_f32_e32 v227, v227
	s_nop 0
	v_fma_f32 v236, -v236, v227, v227
	v_cvt_pk_f16_f32 v247, v236, v231
	ds_write_b64 v250, v[246:247] offset:12288
	v_mfma_f32_16x16x32_f16 v[210:213], v[66:69], v[154:157], v[210:213]
	v_mfma_f32_16x16x32_f16 v[214:217], v[78:81], v[154:157], v[214:217]
	buffer_load_dwordx2 v[192:193], v209, s[56:59], s45 offen
	s_waitcnt lgkmcnt(0)
	s_barrier
	ds_read_b128 v[158:161], v248 offset:4096
	ds_read_b128 v[162:165], v248 offset:5120
	ds_read_b128 v[166:169], v249 offset:6144
	ds_read_b128 v[170:173], v249 offset:7168
	v_mfma_f32_16x16x32_f16 v[218:221], v[82:85], v[150:153], v[106:109]
	v_mfma_f32_16x16x32_f16 v[222:225], v[90:93], v[150:153], v[110:113]
	v_mfma_f32_16x16x32_f16 v[218:221], v[86:89], v[154:157], v[218:221]
	v_mfma_f32_16x16x32_f16 v[222:225], v[94:97], v[154:157], v[222:225]
	s_waitcnt lgkmcnt(2)
	v_mfma_f32_16x16x32_f16 v[210:213], v[54:57], v[158:161], v[210:213]
	v_mfma_f32_16x16x32_f16 v[210:213], v[58:61], v[162:165], v[210:213]
	s_waitcnt lgkmcnt(0)
	v_mfma_f32_16x16x32_f16 v[210:213], v[62:65], v[166:169], v[210:213]
	v_mfma_f32_16x16x32_f16 v[210:213], v[50:53], v[170:173], v[210:213]
	s_waitcnt vmcnt(9)
	v_cvt_pk_f16_f32 v251, v190, v191
	ds_write_b32 v1, v251 offset:2048
	ds_read_b128 v[150:153], v186 offset:0
	ds_read_b128 v[154:157], v186 offset:1024
	s_nop 2
	v_exp_f32_e32 v226, v210
	v_exp_f32_e32 v227, v211
	v_mfma_f32_16x16x32_f16 v[214:217], v[34:37], v[158:161], v[214:217]
	v_min_f32_e32 v228, s42, v212
	v_exp_f32_e32 v229, v213
	v_mfma_f32_16x16x32_f16 v[214:217], v[38:41], v[162:165], v[214:217]
	v_exp_f32_e32 v228, v228
	v_add_f32_e32 v227, 1.0, v227
	v_mfma_f32_16x16x32_f16 v[214:217], v[42:45], v[166:169], v[214:217]
	v_fma_f32 v230, v228, s41, s41
	v_rcp_f32_e32 v227, v227
	v_mfma_f32_16x16x32_f16 v[214:217], v[46:49], v[170:173], v[214:217]
	v_fma_f32 v230, v226, v230, v230
	v_rcp_f32_e32 v230, v230
	v_mfma_f32_16x16x32_f16 v[218:221], v[18:21], v[158:161], v[218:221]
	v_fma_f32 v226, -v228, v230, v230
	v_fma_f32 v200, v200, v227, v226
	v_mfma_f32_16x16x32_f16 v[218:221], v[14:17], v[162:165], v[218:221]
	v_exp_f32_e32 v226, v200
	s_nop 0
	v_add_f32_e32 v227, 1.0, v226
	v_mfma_f32_16x16x32_f16 v[218:221], v[10:13], v[166:169], v[218:221]
	v_fma_f32 v227, v229, v227, v227
	v_rcp_f32_e32 v227, v227
	v_mfma_f32_16x16x32_f16 v[218:221], v[26:29], v[170:173], v[218:221]
	v_fma_f32 v226, -v226, v227, v227
	v_exp_f32_e32 v231, v214
	v_mfma_f32_16x16x32_f16 v[222:225], v[2:5], v[158:161], v[222:225]
	v_exp_f32_e32 v232, v215
	v_min_f32_e32 v233, s42, v216
	v_mfma_f32_16x16x32_f16 v[222:225], v[6:9], v[162:165], v[222:225]
	v_exp_f32_e32 v234, v217
	v_exp_f32_e32 v233, v233
	v_mfma_f32_16x16x32_f16 v[222:225], v[22:25], v[166:169], v[222:225]
	v_exp_f32_e32 v236, v218
	v_add_f32_e32 v232, 1.0, v232
	v_mfma_f32_16x16x32_f16 v[222:225], v[30:33], v[170:173], v[222:225]
	v_fma_f32 v235, v233, s41, s41
	v_exp_f32_e32 v227, v219
	v_rcp_f32_e32 v232, v232
	v_fma_f32 v235, v231, v235, v235
	v_min_f32_e32 v228, s42, v220
	v_rcp_f32_e32 v235, v235
	s_nop 0
	v_fma_f32 v231, -v233, v235, v235
	v_exp_f32_e32 v229, v221
	v_fma_f32 v201, v201, v232, v231
	v_exp_f32_e32 v231, v201
	v_exp_f32_e32 v228, v228
	v_add_f32_e32 v232, 1.0, v231
	v_fma_f32 v232, v234, v232, v232
	v_add_f32_e32 v227, 1.0, v227
	v_rcp_f32_e32 v232, v232
	v_mfma_f32_16x16x32_f16 v[146:149], v[114:117], v[158:161], v[146:149]
	v_fma_f32 v231, -v231, v232, v232
	v_fma_f32 v230, v228, s41, s41
	v_cvt_pk_f16_f32 v246, v226, v231
	v_mfma_f32_16x16x32_f16 v[146:149], v[118:121], v[162:165], v[146:149]
	v_exp_f32_e32 v231, v222
	v_rcp_f32_e32 v227, v227
	v_exp_f32_e32 v232, v223
	buffer_load_dwordx4 v[114:117], v189, s[80:83], s46 offen
	buffer_load_dwordx4 v[118:121], v208, s[80:83], s46 offen
	v_min_f32_e32 v233, s42, v224
	v_fma_f32 v230, v236, v230, v230
	v_exp_f32_e32 v234, v225
	s_waitcnt lgkmcnt(0)
	v_mfma_f32_16x16x32_f16 v[210:213], v[70:73], v[150:153], v[98:101]
	v_exp_f32_e32 v233, v233
	v_rcp_f32_e32 v230, v230
	v_add_f32_e32 v232, 1.0, v232
	v_mfma_f32_16x16x32_f16 v[214:217], v[74:77], v[150:153], v[102:105]
	v_fma_f32 v235, v233, s41, s41
	v_fma_f32 v236, -v228, v230, v230
	v_rcp_f32_e32 v232, v232
	v_fma_f32 v235, v231, v235, v235
	v_fma_f32 v198, v198, v227, v236
	v_rcp_f32_e32 v235, v235
	s_nop 0
	v_fma_f32 v231, -v233, v235, v235
	v_exp_f32_e32 v236, v198
	v_fma_f32 v199, v199, v232, v231
	v_exp_f32_e32 v231, v199
	v_add_f32_e32 v227, 1.0, v236
	v_add_f32_e32 v232, 1.0, v231
	v_fma_f32 v232, v234, v232, v232
	v_fma_f32 v227, v229, v227, v227
	v_rcp_f32_e32 v232, v232
	s_nop 0
	v_fma_f32 v231, -v231, v232, v232
	v_rcp_f32_e32 v227, v227
	s_nop 0
	v_fma_f32 v236, -v236, v227, v227
	v_cvt_pk_f16_f32 v247, v236, v231
	ds_write_b64 v250, v[246:247] offset:16384
	v_mfma_f32_16x16x32_f16 v[210:213], v[66:69], v[154:157], v[210:213]
	v_mfma_f32_16x16x32_f16 v[214:217], v[78:81], v[154:157], v[214:217]
	buffer_load_dwordx2 v[190:191], v209, s[60:63], s45 offen
	s_add_i32 s45, s45, 0x400000
	s_add_i32 s46, s46, 0x10000
	s_waitcnt lgkmcnt(0)
	s_barrier
	ds_read_b128 v[158:161], v248 offset:8192
	ds_read_b128 v[162:165], v248 offset:9216
	ds_read_b128 v[166:169], v249 offset:10240
	ds_read_b128 v[170:173], v249 offset:11264
	v_mfma_f32_16x16x32_f16 v[218:221], v[82:85], v[150:153], v[106:109]
	v_mfma_f32_16x16x32_f16 v[222:225], v[90:93], v[150:153], v[110:113]
	v_mfma_f32_16x16x32_f16 v[218:221], v[86:89], v[154:157], v[218:221]
	v_mfma_f32_16x16x32_f16 v[222:225], v[94:97], v[154:157], v[222:225]
	s_waitcnt lgkmcnt(2)
	v_mfma_f32_16x16x32_f16 v[210:213], v[54:57], v[158:161], v[210:213]
	v_mfma_f32_16x16x32_f16 v[210:213], v[58:61], v[162:165], v[210:213]
	s_waitcnt lgkmcnt(0)
	v_mfma_f32_16x16x32_f16 v[210:213], v[62:65], v[166:169], v[210:213]
	v_mfma_f32_16x16x32_f16 v[210:213], v[50:53], v[170:173], v[210:213]
	s_waitcnt vmcnt(9)
	v_cvt_pk_f16_f32 v251, v196, v197
	ds_write_b32 v1, v251 offset:4096
	ds_read_b128 v[150:153], v186 offset:2048
	ds_read_b128 v[154:157], v186 offset:3072
	s_nop 2
	v_exp_f32_e32 v226, v210
	v_exp_f32_e32 v227, v211
	v_mfma_f32_16x16x32_f16 v[214:217], v[34:37], v[158:161], v[214:217]
	v_min_f32_e32 v228, s42, v212
	v_exp_f32_e32 v229, v213
	v_mfma_f32_16x16x32_f16 v[214:217], v[38:41], v[162:165], v[214:217]
	v_exp_f32_e32 v228, v228
	v_add_f32_e32 v227, 1.0, v227
	v_mfma_f32_16x16x32_f16 v[214:217], v[42:45], v[166:169], v[214:217]
	v_fma_f32 v230, v228, s41, s41
	v_rcp_f32_e32 v227, v227
	v_mfma_f32_16x16x32_f16 v[214:217], v[46:49], v[170:173], v[214:217]
	v_fma_f32 v230, v226, v230, v230
	v_rcp_f32_e32 v230, v230
	v_mfma_f32_16x16x32_f16 v[218:221], v[18:21], v[158:161], v[218:221]
	v_fma_f32 v226, -v228, v230, v230
	v_fma_f32 v200, v200, v227, v226
	v_mfma_f32_16x16x32_f16 v[218:221], v[14:17], v[162:165], v[218:221]
	v_exp_f32_e32 v226, v200
	s_nop 0
	v_add_f32_e32 v227, 1.0, v226
	v_mfma_f32_16x16x32_f16 v[218:221], v[10:13], v[166:169], v[218:221]
	v_fma_f32 v227, v229, v227, v227
	v_rcp_f32_e32 v227, v227
	v_mfma_f32_16x16x32_f16 v[218:221], v[26:29], v[170:173], v[218:221]
	v_fma_f32 v226, -v226, v227, v227
	v_exp_f32_e32 v231, v214
	v_mfma_f32_16x16x32_f16 v[222:225], v[2:5], v[158:161], v[222:225]
	v_exp_f32_e32 v232, v215
	v_min_f32_e32 v233, s42, v216
	v_mfma_f32_16x16x32_f16 v[222:225], v[6:9], v[162:165], v[222:225]
	v_exp_f32_e32 v234, v217
	v_exp_f32_e32 v233, v233
	v_mfma_f32_16x16x32_f16 v[222:225], v[22:25], v[166:169], v[222:225]
	v_exp_f32_e32 v236, v218
	v_add_f32_e32 v232, 1.0, v232
	v_mfma_f32_16x16x32_f16 v[222:225], v[30:33], v[170:173], v[222:225]
	v_fma_f32 v235, v233, s41, s41
	v_exp_f32_e32 v227, v219
	v_rcp_f32_e32 v232, v232
	v_fma_f32 v235, v231, v235, v235
	v_min_f32_e32 v228, s42, v220
	v_rcp_f32_e32 v235, v235
	s_nop 0
	v_fma_f32 v231, -v233, v235, v235
	v_exp_f32_e32 v229, v221
	v_fma_f32 v201, v201, v232, v231
	v_exp_f32_e32 v231, v201
	v_exp_f32_e32 v228, v228
	v_add_f32_e32 v232, 1.0, v231
	v_fma_f32 v232, v234, v232, v232
	v_add_f32_e32 v227, 1.0, v227
	v_rcp_f32_e32 v232, v232
	v_mfma_f32_16x16x32_f16 v[146:149], v[138:141], v[158:161], v[146:149]
	v_fma_f32 v231, -v231, v232, v232
	v_fma_f32 v230, v228, s41, s41
	v_cvt_pk_f16_f32 v246, v226, v231
	v_mfma_f32_16x16x32_f16 v[146:149], v[142:145], v[162:165], v[146:149]
	v_exp_f32_e32 v231, v222
	v_rcp_f32_e32 v227, v227
	v_exp_f32_e32 v232, v223
	buffer_load_dwordx4 v[138:141], v189, s[68:71], s46 offen
	buffer_load_dwordx4 v[142:145], v208, s[68:71], s46 offen
	v_min_f32_e32 v233, s42, v224
	v_fma_f32 v230, v236, v230, v230
	v_exp_f32_e32 v234, v225
	s_waitcnt lgkmcnt(0)
	v_mfma_f32_16x16x32_f16 v[210:213], v[70:73], v[150:153], v[98:101]
	v_exp_f32_e32 v233, v233
	v_rcp_f32_e32 v230, v230
	v_add_f32_e32 v232, 1.0, v232
	v_mfma_f32_16x16x32_f16 v[214:217], v[74:77], v[150:153], v[102:105]
	v_fma_f32 v235, v233, s41, s41
	v_fma_f32 v236, -v228, v230, v230
	v_rcp_f32_e32 v232, v232
	v_fma_f32 v235, v231, v235, v235
	v_fma_f32 v198, v198, v227, v236
	v_rcp_f32_e32 v235, v235
	s_nop 0
	v_fma_f32 v231, -v233, v235, v235
	v_exp_f32_e32 v236, v198
	v_fma_f32 v199, v199, v232, v231
	v_exp_f32_e32 v231, v199
	v_add_f32_e32 v227, 1.0, v236
	v_add_f32_e32 v232, 1.0, v231
	v_fma_f32 v232, v234, v232, v232
	v_fma_f32 v227, v229, v227, v227
	v_rcp_f32_e32 v232, v232
	s_nop 0
	v_fma_f32 v231, -v231, v232, v232
	v_rcp_f32_e32 v227, v227
	s_nop 0
	v_fma_f32 v236, -v236, v227, v227
	v_cvt_pk_f16_f32 v247, v236, v231
	ds_write_b64 v250, v[246:247] offset:20480
	v_mfma_f32_16x16x32_f16 v[210:213], v[66:69], v[154:157], v[210:213]
	v_mfma_f32_16x16x32_f16 v[214:217], v[78:81], v[154:157], v[214:217]
	buffer_load_dwordx2 v[196:197], v209, s[48:51], s45 offen
	s_waitcnt lgkmcnt(0)
	s_barrier
	ds_read_b128 v[158:161], v248 offset:12288
	ds_read_b128 v[162:165], v248 offset:13312
	ds_read_b128 v[166:169], v249 offset:14336
	ds_read_b128 v[170:173], v249 offset:15360
	v_mfma_f32_16x16x32_f16 v[218:221], v[82:85], v[150:153], v[106:109]
	v_mfma_f32_16x16x32_f16 v[222:225], v[90:93], v[150:153], v[110:113]
	v_mfma_f32_16x16x32_f16 v[218:221], v[86:89], v[154:157], v[218:221]
	v_mfma_f32_16x16x32_f16 v[222:225], v[94:97], v[154:157], v[222:225]
	s_waitcnt lgkmcnt(2)
	v_mfma_f32_16x16x32_f16 v[210:213], v[54:57], v[158:161], v[210:213]
	v_mfma_f32_16x16x32_f16 v[210:213], v[58:61], v[162:165], v[210:213]
	s_waitcnt lgkmcnt(0)
	v_mfma_f32_16x16x32_f16 v[210:213], v[62:65], v[166:169], v[210:213]
	v_mfma_f32_16x16x32_f16 v[210:213], v[50:53], v[170:173], v[210:213]
	s_waitcnt vmcnt(9)
	v_cvt_pk_f16_f32 v251, v194, v195
	ds_write_b32 v1, v251 offset:6144
	ds_read_b128 v[150:153], v186 offset:4096
	ds_read_b128 v[154:157], v186 offset:5120
	s_nop 2
	v_exp_f32_e32 v226, v210
	v_exp_f32_e32 v227, v211
	v_mfma_f32_16x16x32_f16 v[214:217], v[34:37], v[158:161], v[214:217]
	v_min_f32_e32 v228, s42, v212
	v_exp_f32_e32 v229, v213
	v_mfma_f32_16x16x32_f16 v[214:217], v[38:41], v[162:165], v[214:217]
	v_exp_f32_e32 v228, v228
	v_add_f32_e32 v227, 1.0, v227
	v_mfma_f32_16x16x32_f16 v[214:217], v[42:45], v[166:169], v[214:217]
	v_fma_f32 v230, v228, s41, s41
	v_rcp_f32_e32 v227, v227
	v_mfma_f32_16x16x32_f16 v[214:217], v[46:49], v[170:173], v[214:217]
	v_fma_f32 v230, v226, v230, v230
	v_rcp_f32_e32 v230, v230
	v_mfma_f32_16x16x32_f16 v[218:221], v[18:21], v[158:161], v[218:221]
	v_fma_f32 v226, -v228, v230, v230
	v_fma_f32 v200, v200, v227, v226
	v_mfma_f32_16x16x32_f16 v[218:221], v[14:17], v[162:165], v[218:221]
	v_exp_f32_e32 v226, v200
	s_nop 0
	v_add_f32_e32 v227, 1.0, v226
	v_mfma_f32_16x16x32_f16 v[218:221], v[10:13], v[166:169], v[218:221]
	v_fma_f32 v227, v229, v227, v227
	v_rcp_f32_e32 v227, v227
	v_mfma_f32_16x16x32_f16 v[218:221], v[26:29], v[170:173], v[218:221]
	v_fma_f32 v226, -v226, v227, v227
	v_exp_f32_e32 v231, v214
	v_mfma_f32_16x16x32_f16 v[222:225], v[2:5], v[158:161], v[222:225]
	v_exp_f32_e32 v232, v215
	v_min_f32_e32 v233, s42, v216
	v_mfma_f32_16x16x32_f16 v[222:225], v[6:9], v[162:165], v[222:225]
	v_exp_f32_e32 v234, v217
	v_exp_f32_e32 v233, v233
	v_mfma_f32_16x16x32_f16 v[222:225], v[22:25], v[166:169], v[222:225]
	v_exp_f32_e32 v236, v218
	v_add_f32_e32 v232, 1.0, v232
	v_mfma_f32_16x16x32_f16 v[222:225], v[30:33], v[170:173], v[222:225]
	v_fma_f32 v235, v233, s41, s41
	v_exp_f32_e32 v227, v219
	v_rcp_f32_e32 v232, v232
	v_fma_f32 v235, v231, v235, v235
	v_min_f32_e32 v228, s42, v220
	v_rcp_f32_e32 v235, v235
	s_nop 0
	v_fma_f32 v231, -v233, v235, v235
	v_exp_f32_e32 v229, v221
	v_fma_f32 v201, v201, v232, v231
	v_exp_f32_e32 v231, v201
	v_exp_f32_e32 v228, v228
	v_add_f32_e32 v232, 1.0, v231
	v_fma_f32 v232, v234, v232, v232
	v_add_f32_e32 v227, 1.0, v227
	v_rcp_f32_e32 v232, v232
	v_mfma_f32_16x16x32_f16 v[146:149], v[130:133], v[158:161], v[146:149]
	v_fma_f32 v231, -v231, v232, v232
	v_fma_f32 v230, v228, s41, s41
	v_cvt_pk_f16_f32 v246, v226, v231
	v_mfma_f32_16x16x32_f16 v[146:149], v[134:137], v[162:165], v[146:149]
	v_exp_f32_e32 v231, v222
	v_rcp_f32_e32 v227, v227
	v_exp_f32_e32 v232, v223
	buffer_load_dwordx4 v[130:133], v189, s[72:75], s46 offen
	buffer_load_dwordx4 v[134:137], v208, s[72:75], s46 offen
	v_min_f32_e32 v233, s42, v224
	v_fma_f32 v230, v236, v230, v230
	v_exp_f32_e32 v234, v225
	s_waitcnt lgkmcnt(0)
	v_mfma_f32_16x16x32_f16 v[210:213], v[70:73], v[150:153], v[98:101]
	v_exp_f32_e32 v233, v233
	v_rcp_f32_e32 v230, v230
	v_add_f32_e32 v232, 1.0, v232
	v_mfma_f32_16x16x32_f16 v[214:217], v[74:77], v[150:153], v[102:105]
	v_fma_f32 v235, v233, s41, s41
	v_fma_f32 v236, -v228, v230, v230
	v_rcp_f32_e32 v232, v232
	v_fma_f32 v235, v231, v235, v235
	v_fma_f32 v198, v198, v227, v236
	v_rcp_f32_e32 v235, v235
	s_nop 0
	v_fma_f32 v231, -v233, v235, v235
	v_exp_f32_e32 v236, v198
	v_fma_f32 v199, v199, v232, v231
	v_exp_f32_e32 v231, v199
	v_add_f32_e32 v227, 1.0, v236
	v_add_f32_e32 v232, 1.0, v231
	v_fma_f32 v232, v234, v232, v232
	v_fma_f32 v227, v229, v227, v227
	v_rcp_f32_e32 v232, v232
	s_nop 0
	v_fma_f32 v231, -v231, v232, v232
	v_rcp_f32_e32 v227, v227
	s_nop 0
	v_fma_f32 v236, -v236, v227, v227
	v_cvt_pk_f16_f32 v247, v236, v231
	ds_write_b64 v250, v[246:247] offset:24576
	v_mfma_f32_16x16x32_f16 v[210:213], v[66:69], v[154:157], v[210:213]
	v_mfma_f32_16x16x32_f16 v[214:217], v[78:81], v[154:157], v[214:217]
	buffer_load_dwordx2 v[194:195], v209, s[52:55], s45 offen
	v_add_u32_e32 v250, 0x4000, v250
	v_add_u32_e32 v248, 0x4000, v248
	v_add_u32_e32 v249, 0x4000, v249
	s_waitcnt lgkmcnt(0)
	s_barrier
	s_cmp_lt_u32 s46, 0xa0000
	s_cbranch_scc1 .Lmy_loopb
	ds_read_b128 v[158:161], v248 offset:0
	ds_read_b128 v[162:165], v248 offset:1024
	ds_read_b128 v[166:169], v249 offset:2048
	ds_read_b128 v[170:173], v249 offset:3072
	v_mfma_f32_16x16x32_f16 v[218:221], v[82:85], v[150:153], v[106:109]
	v_mfma_f32_16x16x32_f16 v[222:225], v[90:93], v[150:153], v[110:113]
	v_mfma_f32_16x16x32_f16 v[218:221], v[86:89], v[154:157], v[218:221]
	v_mfma_f32_16x16x32_f16 v[222:225], v[94:97], v[154:157], v[222:225]
	s_waitcnt lgkmcnt(2)
	v_mfma_f32_16x16x32_f16 v[210:213], v[54:57], v[158:161], v[210:213]
	v_mfma_f32_16x16x32_f16 v[210:213], v[58:61], v[162:165], v[210:213]
	s_waitcnt lgkmcnt(0)
	v_mfma_f32_16x16x32_f16 v[210:213], v[62:65], v[166:169], v[210:213]
	v_mfma_f32_16x16x32_f16 v[210:213], v[50:53], v[170:173], v[210:213]
	s_waitcnt vmcnt(9)
	v_cvt_pk_f16_f32 v251, v192, v193
	ds_write_b32 v1, v251 offset:0
	ds_read_b128 v[150:153], v186 offset:6144
	ds_read_b128 v[154:157], v186 offset:7168
	s_nop 2
	v_exp_f32_e32 v226, v210
	v_exp_f32_e32 v227, v211
	v_mfma_f32_16x16x32_f16 v[214:217], v[34:37], v[158:161], v[214:217]
	v_min_f32_e32 v228, s42, v212
	v_exp_f32_e32 v229, v213
	v_mfma_f32_16x16x32_f16 v[214:217], v[38:41], v[162:165], v[214:217]
	v_exp_f32_e32 v228, v228
	v_add_f32_e32 v227, 1.0, v227
	v_mfma_f32_16x16x32_f16 v[214:217], v[42:45], v[166:169], v[214:217]
	v_fma_f32 v230, v228, s41, s41
	v_rcp_f32_e32 v227, v227
	v_mfma_f32_16x16x32_f16 v[214:217], v[46:49], v[170:173], v[214:217]
	v_fma_f32 v230, v226, v230, v230
	v_rcp_f32_e32 v230, v230
	v_mfma_f32_16x16x32_f16 v[218:221], v[18:21], v[158:161], v[218:221]
	v_fma_f32 v226, -v228, v230, v230
	v_fma_f32 v200, v200, v227, v226
	v_mfma_f32_16x16x32_f16 v[218:221], v[14:17], v[162:165], v[218:221]
	v_min_f32_e32 v226, s42, v200
	v_exp_f32_e32 v226, v226
	v_mfma_f32_16x16x32_f16 v[218:221], v[10:13], v[166:169], v[218:221]
	v_add_f32_e32 v227, 1.0, v226
	v_fma_f32 v227, v229, v227, v227
	v_mfma_f32_16x16x32_f16 v[218:221], v[26:29], v[170:173], v[218:221]
	v_rcp_f32_e32 v227, v227
	v_exp_f32_e32 v231, v214
	v_mfma_f32_16x16x32_f16 v[222:225], v[2:5], v[158:161], v[222:225]
	v_exp_f32_e32 v232, v215
	v_fma_f32 v226, -v226, v227, v227
	v_mfma_f32_16x16x32_f16 v[222:225], v[6:9], v[162:165], v[222:225]
	v_min_f32_e32 v233, s42, v216
	v_exp_f32_e32 v234, v217
	v_mfma_f32_16x16x32_f16 v[222:225], v[22:25], v[166:169], v[222:225]
	v_exp_f32_e32 v236, v218
	v_exp_f32_e32 v233, v233
	v_mfma_f32_16x16x32_f16 v[222:225], v[30:33], v[170:173], v[222:225]
	v_add_f32_e32 v232, 1.0, v232
	v_exp_f32_e32 v227, v219
	v_fma_f32 v235, v233, s41, s41
	v_rcp_f32_e32 v232, v232
	v_min_f32_e32 v228, s42, v220
	v_fma_f32 v235, v231, v235, v235
	v_rcp_f32_e32 v235, v235
	v_exp_f32_e32 v229, v221
	v_fma_f32 v231, -v233, v235, v235
	v_fma_f32 v201, v201, v232, v231
	v_exp_f32_e32 v228, v228
	v_min_f32_e32 v231, s42, v201
	v_exp_f32_e32 v231, v231
	v_add_f32_e32 v227, 1.0, v227
	v_add_f32_e32 v232, 1.0, v231
	v_mfma_f32_16x16x32_f16 v[146:149], v[122:125], v[158:161], v[146:149]
	v_fma_f32 v232, v234, v232, v232
	v_fma_f32 v230, v228, s41, s41
	v_rcp_f32_e32 v232, v232
	v_mfma_f32_16x16x32_f16 v[146:149], v[126:129], v[162:165], v[146:149]
	v_fma_f32 v231, -v231, v232, v232
	v_rcp_f32_e32 v227, v227
	v_cvt_pk_f16_f32 v246, v226, v231
	buffer_load_dwordx4 v[122:125], v189, s[76:79], s46 offen
	buffer_load_dwordx4 v[126:129], v208, s[76:79], s46 offen
	v_exp_f32_e32 v231, v222
	v_fma_f32 v230, v236, v230, v230
	v_exp_f32_e32 v232, v223
	s_waitcnt lgkmcnt(0)
	v_mfma_f32_16x16x32_f16 v[210:213], v[70:73], v[150:153], v[98:101]
	v_min_f32_e32 v233, s42, v224
	v_rcp_f32_e32 v230, v230
	v_exp_f32_e32 v234, v225
	v_mfma_f32_16x16x32_f16 v[214:217], v[74:77], v[150:153], v[102:105]
	v_exp_f32_e32 v233, v233
	v_fma_f32 v236, -v228, v230, v230
	v_add_f32_e32 v232, 1.0, v232
	v_fma_f32 v235, v233, s41, s41
	v_fma_f32 v198, v198, v227, v236
	v_rcp_f32_e32 v232, v232
	v_fma_f32 v235, v231, v235, v235
	v_min_f32_e32 v236, s42, v198
	v_rcp_f32_e32 v235, v235
	s_nop 0
	v_fma_f32 v231, -v233, v235, v235
	v_exp_f32_e32 v236, v236
	v_fma_f32 v199, v199, v232, v231
	v_min_f32_e32 v231, s42, v199
	v_add_f32_e32 v227, 1.0, v236
	v_exp_f32_e32 v231, v231
	v_fma_f32 v227, v229, v227, v227
	v_add_f32_e32 v232, 1.0, v231
	v_rcp_f32_e32 v227, v227
	v_fma_f32 v232, v234, v232, v232
	v_fma_f32 v236, -v236, v227, v227
	v_rcp_f32_e32 v232, v232
	s_nop 0
	v_fma_f32 v231, -v231, v232, v232
	v_cvt_pk_f16_f32 v247, v236, v231
	ds_write_b64 v250, v[246:247] offset:12288
	v_mfma_f32_16x16x32_f16 v[210:213], v[66:69], v[154:157], v[210:213]
	v_mfma_f32_16x16x32_f16 v[214:217], v[78:81], v[154:157], v[214:217]
	buffer_load_dwordx2 v[192:193], v209, s[56:59], s45 offen
	s_waitcnt lgkmcnt(0)
	s_barrier
	ds_read_b128 v[158:161], v248 offset:4096
	ds_read_b128 v[162:165], v248 offset:5120
	ds_read_b128 v[166:169], v249 offset:6144
	ds_read_b128 v[170:173], v249 offset:7168
	v_mfma_f32_16x16x32_f16 v[218:221], v[82:85], v[150:153], v[106:109]
	v_mfma_f32_16x16x32_f16 v[222:225], v[90:93], v[150:153], v[110:113]
	v_mfma_f32_16x16x32_f16 v[218:221], v[86:89], v[154:157], v[218:221]
	v_mfma_f32_16x16x32_f16 v[222:225], v[94:97], v[154:157], v[222:225]
	s_waitcnt lgkmcnt(2)
	v_mfma_f32_16x16x32_f16 v[210:213], v[54:57], v[158:161], v[210:213]
	v_mfma_f32_16x16x32_f16 v[210:213], v[58:61], v[162:165], v[210:213]
	s_waitcnt lgkmcnt(0)
	v_mfma_f32_16x16x32_f16 v[210:213], v[62:65], v[166:169], v[210:213]
	v_mfma_f32_16x16x32_f16 v[210:213], v[50:53], v[170:173], v[210:213]
	s_waitcnt vmcnt(9)
	v_cvt_pk_f16_f32 v251, v190, v191
	ds_write_b32 v1, v251 offset:2048
	ds_read_b128 v[150:153], v186 offset:0
	ds_read_b128 v[154:157], v186 offset:1024
	s_nop 2
	v_exp_f32_e32 v226, v210
	v_exp_f32_e32 v227, v211
	v_mfma_f32_16x16x32_f16 v[214:217], v[34:37], v[158:161], v[214:217]
	v_min_f32_e32 v228, s42, v212
	v_exp_f32_e32 v229, v213
	v_mfma_f32_16x16x32_f16 v[214:217], v[38:41], v[162:165], v[214:217]
	v_exp_f32_e32 v228, v228
	v_add_f32_e32 v227, 1.0, v227
	v_mfma_f32_16x16x32_f16 v[214:217], v[42:45], v[166:169], v[214:217]
	v_fma_f32 v230, v228, s41, s41
	v_rcp_f32_e32 v227, v227
	v_mfma_f32_16x16x32_f16 v[214:217], v[46:49], v[170:173], v[214:217]
	v_fma_f32 v230, v226, v230, v230
	v_rcp_f32_e32 v230, v230
	v_mfma_f32_16x16x32_f16 v[218:221], v[18:21], v[158:161], v[218:221]
	v_fma_f32 v226, -v228, v230, v230
	v_fma_f32 v200, v200, v227, v226
	v_mfma_f32_16x16x32_f16 v[218:221], v[14:17], v[162:165], v[218:221]
	v_min_f32_e32 v226, s42, v200
	v_exp_f32_e32 v226, v226
	v_mfma_f32_16x16x32_f16 v[218:221], v[10:13], v[166:169], v[218:221]
	v_add_f32_e32 v227, 1.0, v226
	v_fma_f32 v227, v229, v227, v227
	v_mfma_f32_16x16x32_f16 v[218:221], v[26:29], v[170:173], v[218:221]
	v_rcp_f32_e32 v227, v227
	v_exp_f32_e32 v231, v214
	v_mfma_f32_16x16x32_f16 v[222:225], v[2:5], v[158:161], v[222:225]
	v_exp_f32_e32 v232, v215
	v_fma_f32 v226, -v226, v227, v227
	v_mfma_f32_16x16x32_f16 v[222:225], v[6:9], v[162:165], v[222:225]
	v_min_f32_e32 v233, s42, v216
	v_exp_f32_e32 v234, v217
	v_mfma_f32_16x16x32_f16 v[222:225], v[22:25], v[166:169], v[222:225]
	v_exp_f32_e32 v236, v218
	v_exp_f32_e32 v233, v233
	v_mfma_f32_16x16x32_f16 v[222:225], v[30:33], v[170:173], v[222:225]
	v_add_f32_e32 v232, 1.0, v232
	v_exp_f32_e32 v227, v219
	v_fma_f32 v235, v233, s41, s41
	v_rcp_f32_e32 v232, v232
	v_min_f32_e32 v228, s42, v220
	v_fma_f32 v235, v231, v235, v235
	v_rcp_f32_e32 v235, v235
	v_exp_f32_e32 v229, v221
	v_fma_f32 v231, -v233, v235, v235
	v_fma_f32 v201, v201, v232, v231
	v_exp_f32_e32 v228, v228
	v_min_f32_e32 v231, s42, v201
	v_exp_f32_e32 v231, v231
	v_add_f32_e32 v227, 1.0, v227
	v_add_f32_e32 v232, 1.0, v231
	v_mfma_f32_16x16x32_f16 v[146:149], v[114:117], v[158:161], v[146:149]
	v_fma_f32 v232, v234, v232, v232
	v_fma_f32 v230, v228, s41, s41
	v_rcp_f32_e32 v232, v232
	v_mfma_f32_16x16x32_f16 v[146:149], v[118:121], v[162:165], v[146:149]
	v_fma_f32 v231, -v231, v232, v232
	v_rcp_f32_e32 v227, v227
	v_cvt_pk_f16_f32 v246, v226, v231
	buffer_load_dwordx4 v[114:117], v189, s[80:83], s46 offen
	buffer_load_dwordx4 v[118:121], v208, s[80:83], s46 offen
	v_exp_f32_e32 v231, v222
	v_fma_f32 v230, v236, v230, v230
	v_exp_f32_e32 v232, v223
	s_waitcnt lgkmcnt(0)
	v_mfma_f32_16x16x32_f16 v[210:213], v[70:73], v[150:153], v[98:101]
	v_min_f32_e32 v233, s42, v224
	v_rcp_f32_e32 v230, v230
	v_exp_f32_e32 v234, v225
	v_mfma_f32_16x16x32_f16 v[214:217], v[74:77], v[150:153], v[102:105]
	v_exp_f32_e32 v233, v233
	v_fma_f32 v236, -v228, v230, v230
	v_add_f32_e32 v232, 1.0, v232
	v_fma_f32 v235, v233, s41, s41
	v_fma_f32 v198, v198, v227, v236
	v_rcp_f32_e32 v232, v232
	v_fma_f32 v235, v231, v235, v235
	v_min_f32_e32 v236, s42, v198
	v_rcp_f32_e32 v235, v235
	s_nop 0
	v_fma_f32 v231, -v233, v235, v235
	v_exp_f32_e32 v236, v236
	v_fma_f32 v199, v199, v232, v231
	v_min_f32_e32 v231, s42, v199
	v_add_f32_e32 v227, 1.0, v236
	v_exp_f32_e32 v231, v231
	v_fma_f32 v227, v229, v227, v227
	v_add_f32_e32 v232, 1.0, v231
	v_rcp_f32_e32 v227, v227
	v_fma_f32 v232, v234, v232, v232
	v_fma_f32 v236, -v236, v227, v227
	v_rcp_f32_e32 v232, v232
	s_nop 0
	v_fma_f32 v231, -v231, v232, v232
	v_cvt_pk_f16_f32 v247, v236, v231
	ds_write_b64 v250, v[246:247] offset:16384
	v_mfma_f32_16x16x32_f16 v[210:213], v[66:69], v[154:157], v[210:213]
	v_mfma_f32_16x16x32_f16 v[214:217], v[78:81], v[154:157], v[214:217]
	buffer_load_dwordx2 v[190:191], v209, s[60:63], s45 offen
	s_add_i32 s45, s45, 0x400000
	s_add_i32 s46, s46, 0x10000
	s_waitcnt lgkmcnt(0)
	s_barrier
	ds_read_b128 v[158:161], v248 offset:8192
	ds_read_b128 v[162:165], v248 offset:9216
	ds_read_b128 v[166:169], v249 offset:10240
	ds_read_b128 v[170:173], v249 offset:11264
	v_mfma_f32_16x16x32_f16 v[218:221], v[82:85], v[150:153], v[106:109]
	v_mfma_f32_16x16x32_f16 v[222:225], v[90:93], v[150:153], v[110:113]
	v_mfma_f32_16x16x32_f16 v[218:221], v[86:89], v[154:157], v[218:221]
	v_mfma_f32_16x16x32_f16 v[222:225], v[94:97], v[154:157], v[222:225]
	s_waitcnt lgkmcnt(2)
	v_mfma_f32_16x16x32_f16 v[210:213], v[54:57], v[158:161], v[210:213]
	v_mfma_f32_16x16x32_f16 v[210:213], v[58:61], v[162:165], v[210:213]
	s_waitcnt lgkmcnt(0)
	v_mfma_f32_16x16x32_f16 v[210:213], v[62:65], v[166:169], v[210:213]
	v_mfma_f32_16x16x32_f16 v[210:213], v[50:53], v[170:173], v[210:213]
	s_waitcnt vmcnt(9)
	v_cvt_pk_f16_f32 v251, v196, v197
	ds_write_b32 v1, v251 offset:4096
	ds_read_b128 v[150:153], v186 offset:2048
	ds_read_b128 v[154:157], v186 offset:3072
	s_nop 2
	v_exp_f32_e32 v226, v210
	v_exp_f32_e32 v227, v211
	v_mfma_f32_16x16x32_f16 v[214:217], v[34:37], v[158:161], v[214:217]
	v_min_f32_e32 v228, s42, v212
	v_exp_f32_e32 v229, v213
	v_mfma_f32_16x16x32_f16 v[214:217], v[38:41], v[162:165], v[214:217]
	v_exp_f32_e32 v228, v228
	v_add_f32_e32 v227, 1.0, v227
	v_mfma_f32_16x16x32_f16 v[214:217], v[42:45], v[166:169], v[214:217]
	v_fma_f32 v230, v228, s41, s41
	v_rcp_f32_e32 v227, v227
	v_mfma_f32_16x16x32_f16 v[214:217], v[46:49], v[170:173], v[214:217]
	v_fma_f32 v230, v226, v230, v230
	v_rcp_f32_e32 v230, v230
	v_mfma_f32_16x16x32_f16 v[218:221], v[18:21], v[158:161], v[218:221]
	v_fma_f32 v226, -v228, v230, v230
	v_fma_f32 v200, v200, v227, v226
	v_mfma_f32_16x16x32_f16 v[218:221], v[14:17], v[162:165], v[218:221]
	v_min_f32_e32 v226, s42, v200
	v_exp_f32_e32 v226, v226
	v_mfma_f32_16x16x32_f16 v[218:221], v[10:13], v[166:169], v[218:221]
	v_add_f32_e32 v227, 1.0, v226
	v_fma_f32 v227, v229, v227, v227
	v_mfma_f32_16x16x32_f16 v[218:221], v[26:29], v[170:173], v[218:221]
	v_rcp_f32_e32 v227, v227
	v_exp_f32_e32 v231, v214
	v_mfma_f32_16x16x32_f16 v[222:225], v[2:5], v[158:161], v[222:225]
	v_exp_f32_e32 v232, v215
	v_fma_f32 v226, -v226, v227, v227
	v_mfma_f32_16x16x32_f16 v[222:225], v[6:9], v[162:165], v[222:225]
	v_min_f32_e32 v233, s42, v216
	v_exp_f32_e32 v234, v217
	v_mfma_f32_16x16x32_f16 v[222:225], v[22:25], v[166:169], v[222:225]
	v_exp_f32_e32 v236, v218
	v_exp_f32_e32 v233, v233
	v_mfma_f32_16x16x32_f16 v[222:225], v[30:33], v[170:173], v[222:225]
	v_add_f32_e32 v232, 1.0, v232
	v_exp_f32_e32 v227, v219
	v_fma_f32 v235, v233, s41, s41
	v_rcp_f32_e32 v232, v232
	v_min_f32_e32 v228, s42, v220
	v_fma_f32 v235, v231, v235, v235
	v_rcp_f32_e32 v235, v235
	v_exp_f32_e32 v229, v221
	v_fma_f32 v231, -v233, v235, v235
	v_fma_f32 v201, v201, v232, v231
	v_exp_f32_e32 v228, v228
	v_min_f32_e32 v231, s42, v201
	v_exp_f32_e32 v231, v231
	v_add_f32_e32 v227, 1.0, v227
	v_add_f32_e32 v232, 1.0, v231
	v_mfma_f32_16x16x32_f16 v[146:149], v[138:141], v[158:161], v[146:149]
	v_fma_f32 v232, v234, v232, v232
	v_fma_f32 v230, v228, s41, s41
	v_rcp_f32_e32 v232, v232
	v_mfma_f32_16x16x32_f16 v[146:149], v[142:145], v[162:165], v[146:149]
	v_fma_f32 v231, -v231, v232, v232
	v_rcp_f32_e32 v227, v227
	v_cvt_pk_f16_f32 v246, v226, v231
	buffer_load_dwordx4 v[138:141], v189, s[68:71], s46 offen
	buffer_load_dwordx4 v[142:145], v208, s[68:71], s46 offen
	v_exp_f32_e32 v231, v222
	v_fma_f32 v230, v236, v230, v230
	v_exp_f32_e32 v232, v223
	s_waitcnt lgkmcnt(0)
	v_mfma_f32_16x16x32_f16 v[210:213], v[70:73], v[150:153], v[98:101]
	v_min_f32_e32 v233, s42, v224
	v_rcp_f32_e32 v230, v230
	v_exp_f32_e32 v234, v225
	v_mfma_f32_16x16x32_f16 v[214:217], v[74:77], v[150:153], v[102:105]
	v_exp_f32_e32 v233, v233
	v_fma_f32 v236, -v228, v230, v230
	v_add_f32_e32 v232, 1.0, v232
	v_fma_f32 v235, v233, s41, s41
	v_fma_f32 v198, v198, v227, v236
	v_rcp_f32_e32 v232, v232
	v_fma_f32 v235, v231, v235, v235
	v_min_f32_e32 v236, s42, v198
	v_rcp_f32_e32 v235, v235
	s_nop 0
	v_fma_f32 v231, -v233, v235, v235
	v_exp_f32_e32 v236, v236
	v_fma_f32 v199, v199, v232, v231
	v_min_f32_e32 v231, s42, v199
	v_add_f32_e32 v227, 1.0, v236
	v_exp_f32_e32 v231, v231
	v_fma_f32 v227, v229, v227, v227
	v_add_f32_e32 v232, 1.0, v231
	v_rcp_f32_e32 v227, v227
	v_fma_f32 v232, v234, v232, v232
	v_fma_f32 v236, -v236, v227, v227
	v_rcp_f32_e32 v232, v232
	s_nop 0
	v_fma_f32 v231, -v231, v232, v232
	v_cvt_pk_f16_f32 v247, v236, v231
	ds_write_b64 v250, v[246:247] offset:20480
	v_mfma_f32_16x16x32_f16 v[210:213], v[66:69], v[154:157], v[210:213]
	v_mfma_f32_16x16x32_f16 v[214:217], v[78:81], v[154:157], v[214:217]
	buffer_load_dwordx2 v[196:197], v209, s[48:51], s45 offen
	s_waitcnt lgkmcnt(0)
	s_barrier
	ds_read_b128 v[158:161], v248 offset:12288
	ds_read_b128 v[162:165], v248 offset:13312
	ds_read_b128 v[166:169], v249 offset:14336
	ds_read_b128 v[170:173], v249 offset:15360
	v_mfma_f32_16x16x32_f16 v[218:221], v[82:85], v[150:153], v[106:109]
	v_mfma_f32_16x16x32_f16 v[222:225], v[90:93], v[150:153], v[110:113]
	v_mfma_f32_16x16x32_f16 v[218:221], v[86:89], v[154:157], v[218:221]
	v_mfma_f32_16x16x32_f16 v[222:225], v[94:97], v[154:157], v[222:225]
	s_waitcnt lgkmcnt(2)
	v_mfma_f32_16x16x32_f16 v[210:213], v[54:57], v[158:161], v[210:213]
	v_mfma_f32_16x16x32_f16 v[210:213], v[58:61], v[162:165], v[210:213]
	s_waitcnt lgkmcnt(0)
	v_mfma_f32_16x16x32_f16 v[210:213], v[62:65], v[166:169], v[210:213]
	v_mfma_f32_16x16x32_f16 v[210:213], v[50:53], v[170:173], v[210:213]
	s_waitcnt vmcnt(9)
	v_cvt_pk_f16_f32 v251, v194, v195
	ds_write_b32 v1, v251 offset:6144
	ds_read_b128 v[150:153], v186 offset:4096
	ds_read_b128 v[154:157], v186 offset:5120
	s_nop 2
	v_exp_f32_e32 v226, v210
	v_exp_f32_e32 v227, v211
	v_mfma_f32_16x16x32_f16 v[214:217], v[34:37], v[158:161], v[214:217]
	v_min_f32_e32 v228, s42, v212
	v_exp_f32_e32 v229, v213
	v_mfma_f32_16x16x32_f16 v[214:217], v[38:41], v[162:165], v[214:217]
	v_exp_f32_e32 v228, v228
	v_add_f32_e32 v227, 1.0, v227
	v_mfma_f32_16x16x32_f16 v[214:217], v[42:45], v[166:169], v[214:217]
	v_fma_f32 v230, v228, s41, s41
	v_rcp_f32_e32 v227, v227
	v_mfma_f32_16x16x32_f16 v[214:217], v[46:49], v[170:173], v[214:217]
	v_fma_f32 v230, v226, v230, v230
	v_rcp_f32_e32 v230, v230
	v_mfma_f32_16x16x32_f16 v[218:221], v[18:21], v[158:161], v[218:221]
	v_fma_f32 v226, -v228, v230, v230
	v_fma_f32 v200, v200, v227, v226
	v_mfma_f32_16x16x32_f16 v[218:221], v[14:17], v[162:165], v[218:221]
	v_min_f32_e32 v226, s42, v200
	v_exp_f32_e32 v226, v226
	v_mfma_f32_16x16x32_f16 v[218:221], v[10:13], v[166:169], v[218:221]
	v_add_f32_e32 v227, 1.0, v226
	v_fma_f32 v227, v229, v227, v227
	v_mfma_f32_16x16x32_f16 v[218:221], v[26:29], v[170:173], v[218:221]
	v_rcp_f32_e32 v227, v227
	v_exp_f32_e32 v231, v214
	v_mfma_f32_16x16x32_f16 v[222:225], v[2:5], v[158:161], v[222:225]
	v_exp_f32_e32 v232, v215
	v_fma_f32 v226, -v226, v227, v227
	v_mfma_f32_16x16x32_f16 v[222:225], v[6:9], v[162:165], v[222:225]
	v_min_f32_e32 v233, s42, v216
	v_exp_f32_e32 v234, v217
	v_mfma_f32_16x16x32_f16 v[222:225], v[22:25], v[166:169], v[222:225]
	v_exp_f32_e32 v236, v218
	v_exp_f32_e32 v233, v233
	v_mfma_f32_16x16x32_f16 v[222:225], v[30:33], v[170:173], v[222:225]
	v_add_f32_e32 v232, 1.0, v232
	v_exp_f32_e32 v227, v219
	v_fma_f32 v235, v233, s41, s41
	v_rcp_f32_e32 v232, v232
	v_min_f32_e32 v228, s42, v220
	v_fma_f32 v235, v231, v235, v235
	v_rcp_f32_e32 v235, v235
	v_exp_f32_e32 v229, v221
	v_fma_f32 v231, -v233, v235, v235
	v_fma_f32 v201, v201, v232, v231
	v_exp_f32_e32 v228, v228
	v_min_f32_e32 v231, s42, v201
	v_exp_f32_e32 v231, v231
	v_add_f32_e32 v227, 1.0, v227
	v_add_f32_e32 v232, 1.0, v231
	v_mfma_f32_16x16x32_f16 v[146:149], v[130:133], v[158:161], v[146:149]
	v_fma_f32 v232, v234, v232, v232
	v_fma_f32 v230, v228, s41, s41
	v_rcp_f32_e32 v232, v232
	v_mfma_f32_16x16x32_f16 v[146:149], v[134:137], v[162:165], v[146:149]
	v_fma_f32 v231, -v231, v232, v232
	v_rcp_f32_e32 v227, v227
	v_cvt_pk_f16_f32 v246, v226, v231
	buffer_load_dwordx4 v[130:133], v189, s[72:75], s46 offen
	buffer_load_dwordx4 v[134:137], v208, s[72:75], s46 offen
	v_exp_f32_e32 v231, v222
	v_fma_f32 v230, v236, v230, v230
	v_exp_f32_e32 v232, v223
	s_waitcnt lgkmcnt(0)
	v_mfma_f32_16x16x32_f16 v[210:213], v[70:73], v[150:153], v[98:101]
	v_min_f32_e32 v233, s42, v224
	v_rcp_f32_e32 v230, v230
	v_exp_f32_e32 v234, v225
	v_mfma_f32_16x16x32_f16 v[214:217], v[74:77], v[150:153], v[102:105]
	v_exp_f32_e32 v233, v233
	v_fma_f32 v236, -v228, v230, v230
	v_add_f32_e32 v232, 1.0, v232
	v_fma_f32 v235, v233, s41, s41
	v_fma_f32 v198, v198, v227, v236
	v_rcp_f32_e32 v232, v232
	v_fma_f32 v235, v231, v235, v235
	v_min_f32_e32 v236, s42, v198
	v_rcp_f32_e32 v235, v235
	s_nop 0
	v_fma_f32 v231, -v233, v235, v235
	v_exp_f32_e32 v236, v236
	v_fma_f32 v199, v199, v232, v231
	v_min_f32_e32 v231, s42, v199
	v_add_f32_e32 v227, 1.0, v236
	v_exp_f32_e32 v231, v231
	v_fma_f32 v227, v229, v227, v227
	v_add_f32_e32 v232, 1.0, v231
	v_rcp_f32_e32 v227, v227
	v_fma_f32 v232, v234, v232, v232
	v_fma_f32 v236, -v236, v227, v227
	v_rcp_f32_e32 v232, v232
	s_nop 0
	v_fma_f32 v231, -v231, v232, v232
	v_cvt_pk_f16_f32 v247, v236, v231
	ds_write_b64 v250, v[246:247] offset:24576
	v_mfma_f32_16x16x32_f16 v[210:213], v[66:69], v[154:157], v[210:213]
	v_mfma_f32_16x16x32_f16 v[214:217], v[78:81], v[154:157], v[214:217]
	buffer_load_dwordx2 v[194:195], v209, s[52:55], s45 offen
	v_add_u32_e32 v250, 0x4000, v250
	v_add_u32_e32 v248, 0x4000, v248
	v_add_u32_e32 v249, 0x4000, v249
	s_waitcnt lgkmcnt(0)
	s_barrier
	ds_read_b128 v[158:161], v248 offset:0
	ds_read_b128 v[162:165], v248 offset:1024
	ds_read_b128 v[166:169], v249 offset:2048
	ds_read_b128 v[170:173], v249 offset:3072
	v_mfma_f32_16x16x32_f16 v[218:221], v[82:85], v[150:153], v[106:109]
	v_mfma_f32_16x16x32_f16 v[222:225], v[90:93], v[150:153], v[110:113]
	v_mfma_f32_16x16x32_f16 v[218:221], v[86:89], v[154:157], v[218:221]
	v_mfma_f32_16x16x32_f16 v[222:225], v[94:97], v[154:157], v[222:225]
	s_waitcnt lgkmcnt(2)
	v_mfma_f32_16x16x32_f16 v[210:213], v[54:57], v[158:161], v[210:213]
	v_mfma_f32_16x16x32_f16 v[210:213], v[58:61], v[162:165], v[210:213]
	s_waitcnt lgkmcnt(0)
	v_mfma_f32_16x16x32_f16 v[210:213], v[62:65], v[166:169], v[210:213]
	v_mfma_f32_16x16x32_f16 v[210:213], v[50:53], v[170:173], v[210:213]
	s_waitcnt vmcnt(9)
	v_cvt_pk_f16_f32 v251, v192, v193
	ds_write_b32 v1, v251 offset:0
	ds_read_b128 v[150:153], v186 offset:6144
	ds_read_b128 v[154:157], v186 offset:7168
	s_nop 2
	v_exp_f32_e32 v226, v210
	v_exp_f32_e32 v227, v211
	v_mfma_f32_16x16x32_f16 v[214:217], v[34:37], v[158:161], v[214:217]
	v_min_f32_e32 v228, s42, v212
	v_exp_f32_e32 v229, v213
	v_mfma_f32_16x16x32_f16 v[214:217], v[38:41], v[162:165], v[214:217]
	v_exp_f32_e32 v228, v228
	v_add_f32_e32 v227, 1.0, v227
	v_mfma_f32_16x16x32_f16 v[214:217], v[42:45], v[166:169], v[214:217]
	v_fma_f32 v230, v228, s41, s41
	v_rcp_f32_e32 v227, v227
	v_mfma_f32_16x16x32_f16 v[214:217], v[46:49], v[170:173], v[214:217]
	v_fma_f32 v230, v226, v230, v230
	v_rcp_f32_e32 v230, v230
	v_mfma_f32_16x16x32_f16 v[218:221], v[18:21], v[158:161], v[218:221]
	v_fma_f32 v226, -v228, v230, v230
	v_fma_f32 v200, v200, v227, v226
	v_mfma_f32_16x16x32_f16 v[218:221], v[14:17], v[162:165], v[218:221]
	v_min_f32_e32 v226, s42, v200
	v_exp_f32_e32 v226, v226
	v_mfma_f32_16x16x32_f16 v[218:221], v[10:13], v[166:169], v[218:221]
	v_add_f32_e32 v227, 1.0, v226
	v_fma_f32 v227, v229, v227, v227
	v_mfma_f32_16x16x32_f16 v[218:221], v[26:29], v[170:173], v[218:221]
	v_rcp_f32_e32 v227, v227
	v_exp_f32_e32 v231, v214
	v_mfma_f32_16x16x32_f16 v[222:225], v[2:5], v[158:161], v[222:225]
	v_exp_f32_e32 v232, v215
	v_fma_f32 v226, -v226, v227, v227
	v_mfma_f32_16x16x32_f16 v[222:225], v[6:9], v[162:165], v[222:225]
	v_min_f32_e32 v233, s42, v216
	v_exp_f32_e32 v234, v217
	v_mfma_f32_16x16x32_f16 v[222:225], v[22:25], v[166:169], v[222:225]
	v_exp_f32_e32 v236, v218
	v_exp_f32_e32 v233, v233
	v_mfma_f32_16x16x32_f16 v[222:225], v[30:33], v[170:173], v[222:225]
	v_add_f32_e32 v232, 1.0, v232
	v_exp_f32_e32 v227, v219
	v_fma_f32 v235, v233, s41, s41
	v_rcp_f32_e32 v232, v232
	v_min_f32_e32 v228, s42, v220
	v_fma_f32 v235, v231, v235, v235
	v_rcp_f32_e32 v235, v235
	v_exp_f32_e32 v229, v221
	v_fma_f32 v231, -v233, v235, v235
	v_fma_f32 v201, v201, v232, v231
	v_exp_f32_e32 v228, v228
	v_min_f32_e32 v231, s42, v201
	v_exp_f32_e32 v231, v231
	v_add_f32_e32 v227, 1.0, v227
	v_add_f32_e32 v232, 1.0, v231
	v_mfma_f32_16x16x32_f16 v[146:149], v[122:125], v[158:161], v[146:149]
	v_fma_f32 v232, v234, v232, v232
	v_fma_f32 v230, v228, s41, s41
	v_rcp_f32_e32 v232, v232
	v_mfma_f32_16x16x32_f16 v[146:149], v[126:129], v[162:165], v[146:149]
	v_fma_f32 v231, -v231, v232, v232
	v_rcp_f32_e32 v227, v227
	v_cvt_pk_f16_f32 v246, v226, v231
	buffer_load_dwordx4 v[122:125], v189, s[76:79], s46 offen
	buffer_load_dwordx4 v[126:129], v208, s[76:79], s46 offen
	v_exp_f32_e32 v231, v222
	v_fma_f32 v230, v236, v230, v230
	v_exp_f32_e32 v232, v223
	s_waitcnt lgkmcnt(0)
	v_mfma_f32_16x16x32_f16 v[210:213], v[70:73], v[150:153], v[98:101]
	v_min_f32_e32 v233, s42, v224
	v_rcp_f32_e32 v230, v230
	v_exp_f32_e32 v234, v225
	v_mfma_f32_16x16x32_f16 v[214:217], v[74:77], v[150:153], v[102:105]
	v_exp_f32_e32 v233, v233
	v_fma_f32 v236, -v228, v230, v230
	v_add_f32_e32 v232, 1.0, v232
	v_fma_f32 v235, v233, s41, s41
	v_fma_f32 v198, v198, v227, v236
	v_rcp_f32_e32 v232, v232
	v_fma_f32 v235, v231, v235, v235
	v_min_f32_e32 v236, s42, v198
	v_rcp_f32_e32 v235, v235
	s_nop 0
	v_fma_f32 v231, -v233, v235, v235
	v_exp_f32_e32 v236, v236
	v_fma_f32 v199, v199, v232, v231
	v_min_f32_e32 v231, s42, v199
	v_add_f32_e32 v227, 1.0, v236
	v_exp_f32_e32 v231, v231
	v_fma_f32 v227, v229, v227, v227
	v_add_f32_e32 v232, 1.0, v231
	v_rcp_f32_e32 v227, v227
	v_fma_f32 v232, v234, v232, v232
	v_fma_f32 v236, -v236, v227, v227
	v_rcp_f32_e32 v232, v232
	s_nop 0
	v_fma_f32 v231, -v231, v232, v232
	v_cvt_pk_f16_f32 v247, v236, v231
	ds_write_b64 v250, v[246:247] offset:12288
	v_mfma_f32_16x16x32_f16 v[210:213], v[66:69], v[154:157], v[210:213]
	v_mfma_f32_16x16x32_f16 v[214:217], v[78:81], v[154:157], v[214:217]
	buffer_load_dwordx2 v[192:193], v209, s[56:59], s45 offen
	s_waitcnt lgkmcnt(0)
	s_barrier
	ds_read_b128 v[158:161], v248 offset:4096
	ds_read_b128 v[162:165], v248 offset:5120
	ds_read_b128 v[166:169], v249 offset:6144
	ds_read_b128 v[170:173], v249 offset:7168
	v_mfma_f32_16x16x32_f16 v[218:221], v[82:85], v[150:153], v[106:109]
	v_mfma_f32_16x16x32_f16 v[222:225], v[90:93], v[150:153], v[110:113]
	v_mfma_f32_16x16x32_f16 v[218:221], v[86:89], v[154:157], v[218:221]
	v_mfma_f32_16x16x32_f16 v[222:225], v[94:97], v[154:157], v[222:225]
	s_waitcnt lgkmcnt(2)
	v_mfma_f32_16x16x32_f16 v[210:213], v[54:57], v[158:161], v[210:213]
	v_mfma_f32_16x16x32_f16 v[210:213], v[58:61], v[162:165], v[210:213]
	s_waitcnt lgkmcnt(0)
	v_mfma_f32_16x16x32_f16 v[210:213], v[62:65], v[166:169], v[210:213]
	v_mfma_f32_16x16x32_f16 v[210:213], v[50:53], v[170:173], v[210:213]
	s_waitcnt vmcnt(9)
	v_cvt_pk_f16_f32 v251, v190, v191
	ds_write_b32 v1, v251 offset:2048
	ds_read_b128 v[150:153], v186 offset:0
	ds_read_b128 v[154:157], v186 offset:1024
	s_nop 2
	v_exp_f32_e32 v226, v210
	v_exp_f32_e32 v227, v211
	v_mfma_f32_16x16x32_f16 v[214:217], v[34:37], v[158:161], v[214:217]
	v_min_f32_e32 v228, s42, v212
	v_exp_f32_e32 v229, v213
	v_mfma_f32_16x16x32_f16 v[214:217], v[38:41], v[162:165], v[214:217]
	v_exp_f32_e32 v228, v228
	v_add_f32_e32 v227, 1.0, v227
	v_mfma_f32_16x16x32_f16 v[214:217], v[42:45], v[166:169], v[214:217]
	v_fma_f32 v230, v228, s41, s41
	v_rcp_f32_e32 v227, v227
	v_mfma_f32_16x16x32_f16 v[214:217], v[46:49], v[170:173], v[214:217]
	v_fma_f32 v230, v226, v230, v230
	v_rcp_f32_e32 v230, v230
	v_mfma_f32_16x16x32_f16 v[218:221], v[18:21], v[158:161], v[218:221]
	v_fma_f32 v226, -v228, v230, v230
	v_fma_f32 v200, v200, v227, v226
	v_mfma_f32_16x16x32_f16 v[218:221], v[14:17], v[162:165], v[218:221]
	v_min_f32_e32 v226, s42, v200
	v_exp_f32_e32 v226, v226
	v_mfma_f32_16x16x32_f16 v[218:221], v[10:13], v[166:169], v[218:221]
	v_add_f32_e32 v227, 1.0, v226
	v_fma_f32 v227, v229, v227, v227
	v_mfma_f32_16x16x32_f16 v[218:221], v[26:29], v[170:173], v[218:221]
	v_rcp_f32_e32 v227, v227
	v_exp_f32_e32 v231, v214
	v_mfma_f32_16x16x32_f16 v[222:225], v[2:5], v[158:161], v[222:225]
	v_exp_f32_e32 v232, v215
	v_fma_f32 v226, -v226, v227, v227
	v_mfma_f32_16x16x32_f16 v[222:225], v[6:9], v[162:165], v[222:225]
	v_min_f32_e32 v233, s42, v216
	v_exp_f32_e32 v234, v217
	v_mfma_f32_16x16x32_f16 v[222:225], v[22:25], v[166:169], v[222:225]
	v_exp_f32_e32 v236, v218
	v_exp_f32_e32 v233, v233
	v_mfma_f32_16x16x32_f16 v[222:225], v[30:33], v[170:173], v[222:225]
	v_add_f32_e32 v232, 1.0, v232
	v_exp_f32_e32 v227, v219
	v_fma_f32 v235, v233, s41, s41
	v_rcp_f32_e32 v232, v232
	v_min_f32_e32 v228, s42, v220
	v_fma_f32 v235, v231, v235, v235
	v_rcp_f32_e32 v235, v235
	v_exp_f32_e32 v229, v221
	v_fma_f32 v231, -v233, v235, v235
	v_fma_f32 v201, v201, v232, v231
	v_exp_f32_e32 v228, v228
	v_min_f32_e32 v231, s42, v201
	v_exp_f32_e32 v231, v231
	v_add_f32_e32 v227, 1.0, v227
	v_add_f32_e32 v232, 1.0, v231
	v_mfma_f32_16x16x32_f16 v[146:149], v[114:117], v[158:161], v[146:149]
	v_fma_f32 v232, v234, v232, v232
	v_fma_f32 v230, v228, s41, s41
	v_rcp_f32_e32 v232, v232
	v_mfma_f32_16x16x32_f16 v[146:149], v[118:121], v[162:165], v[146:149]
	v_fma_f32 v231, -v231, v232, v232
	v_rcp_f32_e32 v227, v227
	v_cvt_pk_f16_f32 v246, v226, v231
	buffer_load_dwordx4 v[114:117], v189, s[80:83], s46 offen
	buffer_load_dwordx4 v[118:121], v208, s[80:83], s46 offen
	v_exp_f32_e32 v231, v222
	v_fma_f32 v230, v236, v230, v230
	v_exp_f32_e32 v232, v223
	s_waitcnt lgkmcnt(0)
	v_mfma_f32_16x16x32_f16 v[210:213], v[70:73], v[150:153], v[98:101]
	v_min_f32_e32 v233, s42, v224
	v_rcp_f32_e32 v230, v230
	v_exp_f32_e32 v234, v225
	v_mfma_f32_16x16x32_f16 v[214:217], v[74:77], v[150:153], v[102:105]
	v_exp_f32_e32 v233, v233
	v_fma_f32 v236, -v228, v230, v230
	v_add_f32_e32 v232, 1.0, v232
	v_fma_f32 v235, v233, s41, s41
	v_fma_f32 v198, v198, v227, v236
	v_rcp_f32_e32 v232, v232
	v_fma_f32 v235, v231, v235, v235
	v_min_f32_e32 v236, s42, v198
	v_rcp_f32_e32 v235, v235
	s_nop 0
	v_fma_f32 v231, -v233, v235, v235
	v_exp_f32_e32 v236, v236
	v_fma_f32 v199, v199, v232, v231
	v_min_f32_e32 v231, s42, v199
	v_add_f32_e32 v227, 1.0, v236
	v_exp_f32_e32 v231, v231
	v_fma_f32 v227, v229, v227, v227
	v_add_f32_e32 v232, 1.0, v231
	v_rcp_f32_e32 v227, v227
	v_fma_f32 v232, v234, v232, v232
	v_fma_f32 v236, -v236, v227, v227
	v_rcp_f32_e32 v232, v232
	s_nop 0
	v_fma_f32 v231, -v231, v232, v232
	v_cvt_pk_f16_f32 v247, v236, v231
	ds_write_b64 v250, v[246:247] offset:16384
	v_mfma_f32_16x16x32_f16 v[210:213], v[66:69], v[154:157], v[210:213]
	v_mfma_f32_16x16x32_f16 v[214:217], v[78:81], v[154:157], v[214:217]
	buffer_load_dwordx2 v[190:191], v209, s[60:63], s45 offen
	s_add_i32 s45, s45, 0x400000
	s_add_i32 s46, s46, 0x10000
	s_waitcnt lgkmcnt(0)
	s_barrier
	ds_read_b128 v[158:161], v248 offset:8192
	ds_read_b128 v[162:165], v248 offset:9216
	ds_read_b128 v[166:169], v249 offset:10240
	ds_read_b128 v[170:173], v249 offset:11264
	v_mfma_f32_16x16x32_f16 v[218:221], v[82:85], v[150:153], v[106:109]
	v_mfma_f32_16x16x32_f16 v[222:225], v[90:93], v[150:153], v[110:113]
	v_mfma_f32_16x16x32_f16 v[218:221], v[86:89], v[154:157], v[218:221]
	v_mfma_f32_16x16x32_f16 v[222:225], v[94:97], v[154:157], v[222:225]
	s_waitcnt lgkmcnt(2)
	v_mfma_f32_16x16x32_f16 v[210:213], v[54:57], v[158:161], v[210:213]
	v_mfma_f32_16x16x32_f16 v[210:213], v[58:61], v[162:165], v[210:213]
	s_waitcnt lgkmcnt(0)
	v_mfma_f32_16x16x32_f16 v[210:213], v[62:65], v[166:169], v[210:213]
	v_mfma_f32_16x16x32_f16 v[210:213], v[50:53], v[170:173], v[210:213]
	s_waitcnt vmcnt(9)
	v_cvt_pk_f16_f32 v251, v196, v197
	ds_write_b32 v1, v251 offset:4096
	ds_read_b128 v[150:153], v186 offset:2048
	ds_read_b128 v[154:157], v186 offset:3072
	s_nop 2
	v_exp_f32_e32 v226, v210
	v_exp_f32_e32 v227, v211
	v_mfma_f32_16x16x32_f16 v[214:217], v[34:37], v[158:161], v[214:217]
	v_min_f32_e32 v228, s42, v212
	v_exp_f32_e32 v229, v213
	v_mfma_f32_16x16x32_f16 v[214:217], v[38:41], v[162:165], v[214:217]
	v_exp_f32_e32 v228, v228
	v_add_f32_e32 v227, 1.0, v227
	v_mfma_f32_16x16x32_f16 v[214:217], v[42:45], v[166:169], v[214:217]
	v_fma_f32 v230, v228, s41, s41
	v_rcp_f32_e32 v227, v227
	v_mfma_f32_16x16x32_f16 v[214:217], v[46:49], v[170:173], v[214:217]
	v_fma_f32 v230, v226, v230, v230
	v_rcp_f32_e32 v230, v230
	v_mfma_f32_16x16x32_f16 v[218:221], v[18:21], v[158:161], v[218:221]
	v_fma_f32 v226, -v228, v230, v230
	v_fma_f32 v200, v200, v227, v226
	v_mfma_f32_16x16x32_f16 v[218:221], v[14:17], v[162:165], v[218:221]
	v_min_f32_e32 v226, s42, v200
	v_exp_f32_e32 v226, v226
	v_mfma_f32_16x16x32_f16 v[218:221], v[10:13], v[166:169], v[218:221]
	v_add_f32_e32 v227, 1.0, v226
	v_fma_f32 v227, v229, v227, v227
	v_mfma_f32_16x16x32_f16 v[218:221], v[26:29], v[170:173], v[218:221]
	v_rcp_f32_e32 v227, v227
	v_exp_f32_e32 v231, v214
	v_mfma_f32_16x16x32_f16 v[222:225], v[2:5], v[158:161], v[222:225]
	v_exp_f32_e32 v232, v215
	v_fma_f32 v226, -v226, v227, v227
	v_mfma_f32_16x16x32_f16 v[222:225], v[6:9], v[162:165], v[222:225]
	v_min_f32_e32 v233, s42, v216
	v_exp_f32_e32 v234, v217
	v_mfma_f32_16x16x32_f16 v[222:225], v[22:25], v[166:169], v[222:225]
	v_exp_f32_e32 v236, v218
	v_exp_f32_e32 v233, v233
	v_mfma_f32_16x16x32_f16 v[222:225], v[30:33], v[170:173], v[222:225]
	v_add_f32_e32 v232, 1.0, v232
	v_exp_f32_e32 v227, v219
	v_fma_f32 v235, v233, s41, s41
	v_rcp_f32_e32 v232, v232
	v_min_f32_e32 v228, s42, v220
	v_fma_f32 v235, v231, v235, v235
	v_rcp_f32_e32 v235, v235
	v_exp_f32_e32 v229, v221
	v_fma_f32 v231, -v233, v235, v235
	v_fma_f32 v201, v201, v232, v231
	v_exp_f32_e32 v228, v228
	v_min_f32_e32 v231, s42, v201
	v_exp_f32_e32 v231, v231
	v_add_f32_e32 v227, 1.0, v227
	v_add_f32_e32 v232, 1.0, v231
	v_mfma_f32_16x16x32_f16 v[146:149], v[138:141], v[158:161], v[146:149]
	v_fma_f32 v232, v234, v232, v232
	v_fma_f32 v230, v228, s41, s41
	v_rcp_f32_e32 v232, v232
	v_mfma_f32_16x16x32_f16 v[146:149], v[142:145], v[162:165], v[146:149]
	v_fma_f32 v231, -v231, v232, v232
	v_rcp_f32_e32 v227, v227
	v_cvt_pk_f16_f32 v246, v226, v231
	buffer_load_dwordx4 v[138:141], v189, s[68:71], s46 offen
	buffer_load_dwordx4 v[142:145], v208, s[68:71], s46 offen
	v_exp_f32_e32 v231, v222
	v_fma_f32 v230, v236, v230, v230
	v_exp_f32_e32 v232, v223
	s_waitcnt lgkmcnt(0)
	v_mfma_f32_16x16x32_f16 v[210:213], v[70:73], v[150:153], v[98:101]
	v_min_f32_e32 v233, s42, v224
	v_rcp_f32_e32 v230, v230
	v_exp_f32_e32 v234, v225
	v_mfma_f32_16x16x32_f16 v[214:217], v[74:77], v[150:153], v[102:105]
	v_exp_f32_e32 v233, v233
	v_fma_f32 v236, -v228, v230, v230
	v_add_f32_e32 v232, 1.0, v232
	v_fma_f32 v235, v233, s41, s41
	v_fma_f32 v198, v198, v227, v236
	v_rcp_f32_e32 v232, v232
	v_fma_f32 v235, v231, v235, v235
	v_min_f32_e32 v236, s42, v198
	v_rcp_f32_e32 v235, v235
	s_nop 0
	v_fma_f32 v231, -v233, v235, v235
	v_exp_f32_e32 v236, v236
	v_fma_f32 v199, v199, v232, v231
	v_min_f32_e32 v231, s42, v199
	v_add_f32_e32 v227, 1.0, v236
	v_exp_f32_e32 v231, v231
	v_fma_f32 v227, v229, v227, v227
	v_add_f32_e32 v232, 1.0, v231
	v_rcp_f32_e32 v227, v227
	v_fma_f32 v232, v234, v232, v232
	v_fma_f32 v236, -v236, v227, v227
	v_rcp_f32_e32 v232, v232
	s_nop 0
	v_fma_f32 v231, -v231, v232, v232
	v_cvt_pk_f16_f32 v247, v236, v231
	ds_write_b64 v250, v[246:247] offset:20480
	v_mfma_f32_16x16x32_f16 v[210:213], v[66:69], v[154:157], v[210:213]
	v_mfma_f32_16x16x32_f16 v[214:217], v[78:81], v[154:157], v[214:217]
	buffer_load_dwordx2 v[196:197], v209, s[48:51], s45 offen
	s_waitcnt lgkmcnt(0)
	s_barrier
	ds_read_b128 v[158:161], v248 offset:12288
	ds_read_b128 v[162:165], v248 offset:13312
	ds_read_b128 v[166:169], v249 offset:14336
	ds_read_b128 v[170:173], v249 offset:15360
	v_mfma_f32_16x16x32_f16 v[218:221], v[82:85], v[150:153], v[106:109]
	v_mfma_f32_16x16x32_f16 v[222:225], v[90:93], v[150:153], v[110:113]
	v_mfma_f32_16x16x32_f16 v[218:221], v[86:89], v[154:157], v[218:221]
	v_mfma_f32_16x16x32_f16 v[222:225], v[94:97], v[154:157], v[222:225]
	s_waitcnt lgkmcnt(2)
	v_mfma_f32_16x16x32_f16 v[210:213], v[54:57], v[158:161], v[210:213]
	v_mfma_f32_16x16x32_f16 v[210:213], v[58:61], v[162:165], v[210:213]
	s_waitcnt lgkmcnt(0)
	v_mfma_f32_16x16x32_f16 v[210:213], v[62:65], v[166:169], v[210:213]
	v_mfma_f32_16x16x32_f16 v[210:213], v[50:53], v[170:173], v[210:213]
	s_waitcnt vmcnt(9)
	v_cvt_pk_f16_f32 v251, v194, v195
	ds_write_b32 v1, v251 offset:6144
	ds_read_b128 v[150:153], v186 offset:4096
	ds_read_b128 v[154:157], v186 offset:5120
	s_nop 2
	v_exp_f32_e32 v226, v210
	v_exp_f32_e32 v227, v211
	v_mfma_f32_16x16x32_f16 v[214:217], v[34:37], v[158:161], v[214:217]
	v_min_f32_e32 v228, s42, v212
	v_exp_f32_e32 v229, v213
	v_mfma_f32_16x16x32_f16 v[214:217], v[38:41], v[162:165], v[214:217]
	v_exp_f32_e32 v228, v228
	v_add_f32_e32 v227, 1.0, v227
	v_mfma_f32_16x16x32_f16 v[214:217], v[42:45], v[166:169], v[214:217]
	v_fma_f32 v230, v228, s41, s41
	v_rcp_f32_e32 v227, v227
	v_mfma_f32_16x16x32_f16 v[214:217], v[46:49], v[170:173], v[214:217]
	v_fma_f32 v230, v226, v230, v230
	v_rcp_f32_e32 v230, v230
	v_mfma_f32_16x16x32_f16 v[218:221], v[18:21], v[158:161], v[218:221]
	v_fma_f32 v226, -v228, v230, v230
	v_fma_f32 v200, v200, v227, v226
	v_mfma_f32_16x16x32_f16 v[218:221], v[14:17], v[162:165], v[218:221]
	v_min_f32_e32 v226, s42, v200
	v_exp_f32_e32 v226, v226
	v_mfma_f32_16x16x32_f16 v[218:221], v[10:13], v[166:169], v[218:221]
	v_add_f32_e32 v227, 1.0, v226
	v_fma_f32 v227, v229, v227, v227
	v_mfma_f32_16x16x32_f16 v[218:221], v[26:29], v[170:173], v[218:221]
	v_rcp_f32_e32 v227, v227
	v_exp_f32_e32 v231, v214
	v_mfma_f32_16x16x32_f16 v[222:225], v[2:5], v[158:161], v[222:225]
	v_exp_f32_e32 v232, v215
	v_fma_f32 v226, -v226, v227, v227
	v_mfma_f32_16x16x32_f16 v[222:225], v[6:9], v[162:165], v[222:225]
	v_min_f32_e32 v233, s42, v216
	v_exp_f32_e32 v234, v217
	v_mfma_f32_16x16x32_f16 v[222:225], v[22:25], v[166:169], v[222:225]
	v_exp_f32_e32 v236, v218
	v_exp_f32_e32 v233, v233
	v_mfma_f32_16x16x32_f16 v[222:225], v[30:33], v[170:173], v[222:225]
	v_add_f32_e32 v232, 1.0, v232
	v_exp_f32_e32 v227, v219
	v_fma_f32 v235, v233, s41, s41
	v_rcp_f32_e32 v232, v232
	v_min_f32_e32 v228, s42, v220
	v_fma_f32 v235, v231, v235, v235
	v_rcp_f32_e32 v235, v235
	v_exp_f32_e32 v229, v221
	v_fma_f32 v231, -v233, v235, v235
	v_fma_f32 v201, v201, v232, v231
	v_exp_f32_e32 v228, v228
	v_min_f32_e32 v231, s42, v201
	v_exp_f32_e32 v231, v231
	v_add_f32_e32 v227, 1.0, v227
	v_add_f32_e32 v232, 1.0, v231
	v_mfma_f32_16x16x32_f16 v[146:149], v[130:133], v[158:161], v[146:149]
	v_fma_f32 v232, v234, v232, v232
	v_fma_f32 v230, v228, s41, s41
	v_rcp_f32_e32 v232, v232
	v_mfma_f32_16x16x32_f16 v[146:149], v[134:137], v[162:165], v[146:149]
	v_fma_f32 v231, -v231, v232, v232
	v_rcp_f32_e32 v227, v227
	v_cvt_pk_f16_f32 v246, v226, v231
	buffer_load_dwordx4 v[130:133], v189, s[72:75], s46 offen
	buffer_load_dwordx4 v[134:137], v208, s[72:75], s46 offen
	v_exp_f32_e32 v231, v222
	v_fma_f32 v230, v236, v230, v230
	v_exp_f32_e32 v232, v223
	s_waitcnt lgkmcnt(0)
	v_mfma_f32_16x16x32_f16 v[210:213], v[70:73], v[150:153], v[98:101]
	v_min_f32_e32 v233, s42, v224
	v_rcp_f32_e32 v230, v230
	v_exp_f32_e32 v234, v225
	v_mfma_f32_16x16x32_f16 v[214:217], v[74:77], v[150:153], v[102:105]
	v_exp_f32_e32 v233, v233
	v_fma_f32 v236, -v228, v230, v230
	v_add_f32_e32 v232, 1.0, v232
	v_fma_f32 v235, v233, s41, s41
	v_fma_f32 v198, v198, v227, v236
	v_rcp_f32_e32 v232, v232
	v_fma_f32 v235, v231, v235, v235
	v_min_f32_e32 v236, s42, v198
	v_rcp_f32_e32 v235, v235
	s_nop 0
	v_fma_f32 v231, -v233, v235, v235
	v_exp_f32_e32 v236, v236
	v_fma_f32 v199, v199, v232, v231
	v_min_f32_e32 v231, s42, v199
	v_add_f32_e32 v227, 1.0, v236
	v_exp_f32_e32 v231, v231
	v_fma_f32 v227, v229, v227, v227
	v_add_f32_e32 v232, 1.0, v231
	v_rcp_f32_e32 v227, v227
	v_fma_f32 v232, v234, v232, v232
	v_fma_f32 v236, -v236, v227, v227
	v_rcp_f32_e32 v232, v232
	s_nop 0
	v_fma_f32 v231, -v231, v232, v232
	v_cvt_pk_f16_f32 v247, v236, v231
	ds_write_b64 v250, v[246:247] offset:24576
	v_mfma_f32_16x16x32_f16 v[210:213], v[66:69], v[154:157], v[210:213]
	v_mfma_f32_16x16x32_f16 v[214:217], v[78:81], v[154:157], v[214:217]
	buffer_load_dwordx2 v[194:195], v209, s[52:55], s45 offen
	v_add_u32_e32 v250, 0x4000, v250
	v_add_u32_e32 v248, 0x4000, v248
	v_add_u32_e32 v249, 0x4000, v249
	s_waitcnt lgkmcnt(0)
	s_barrier
	s_nop 7
	ds_read_b128 v[158:161], v248 offset:0
	ds_read_b128 v[162:165], v248 offset:1024
	s_lshr_b32 s48, s35, 5
	v_and_b32_e32 v211, 15, v0
	v_bfe_u32 v212, v0, 4, 2
	v_and_b32_e32 v213, 31, v0
	v_bfe_u32 v214, v0, 5, 1
	v_add_u32_e32 v214, s48, v214
	s_lshl_b32 s49, s35, 4
	s_addk_i32 s49, 0x2000
	v_lshl_add_u32 v215, v212, 8, s49
	v_lshl_add_u32 v215, v211, 2, v215
	v_lshlrev_b32_e32 v216, 6, v213
	v_lshl_add_u32 v216, v214, 2, v216
	v_mul_u32_u24_e32 v217, 0x110, v214
	v_lshl_add_u32 v217, v213, 2, v217
	v_mul_u32_u24_e32 v218, 0x110, v211
	v_add_u32_e32 v219, 0x4000, v206
	v_add_u32_e32 v220, 0x14000, v206
	v_add_u32_e32 v221, 0x24000, v206
	v_add_u32_e32 v222, s34, v211
	v_lshlrev_b32_e32 v222, 9, v222
	v_add_u32_e32 v222, s35, v222
	v_lshl_add_u32 v222, v212, 4, v222
	s_waitcnt vmcnt(10) lgkmcnt(0)
	v_mfma_f32_16x16x32_f16 v[146:149], v[122:125], v[158:161], v[146:149]
	v_mfma_f32_16x16x32_f16 v[146:149], v[126:129], v[162:165], v[146:149]
	ds_read_b64 v[30:31], v219 offset:0
	ds_read_b64 v[32:33], v219 offset:4096
	ds_read_b64 v[34:35], v219 offset:8192
	ds_read_b64 v[36:37], v219 offset:12288
	ds_read_b64 v[38:39], v219 offset:16384
	ds_read_b64 v[40:41], v219 offset:20480
	ds_read_b64 v[42:43], v219 offset:24576
	ds_read_b64 v[44:45], v219 offset:28672
	s_waitcnt lgkmcnt(4)
	ds_read_b64 v[46:47], v219 offset:32768
	ds_read_b64 v[48:49], v219 offset:36864
	ds_read_b64 v[50:51], v219 offset:40960
	ds_read_b64 v[52:53], v219 offset:45056
	ds_read_b64 v[54:55], v219 offset:49152
	ds_read_b64 v[56:57], v219 offset:53248
	ds_read_b64 v[58:59], v219 offset:57344
	ds_read_b64 v[60:61], v219 offset:61440
	s_waitcnt lgkmcnt(4)
	ds_read_b64 v[62:63], v220 offset:0
	ds_read_b64 v[64:65], v220 offset:4096
	ds_read_b64 v[66:67], v220 offset:8192
	ds_read_b64 v[68:69], v220 offset:12288
	ds_read_b64 v[70:71], v220 offset:16384
	ds_read_b64 v[72:73], v220 offset:20480
	ds_read_b64 v[74:75], v220 offset:24576
	ds_read_b64 v[76:77], v220 offset:28672
	s_waitcnt lgkmcnt(4)
	ds_read_b64 v[78:79], v220 offset:32768
	ds_read_b64 v[80:81], v220 offset:36864
	ds_read_b64 v[82:83], v220 offset:40960
	ds_read_b64 v[84:85], v220 offset:45056
	ds_read_b64 v[86:87], v220 offset:49152
	ds_read_b64 v[88:89], v220 offset:53248
	ds_read_b64 v[90:91], v220 offset:57344
	ds_read_b64 v[92:93], v220 offset:61440
	s_waitcnt lgkmcnt(4)
	ds_read_b64 v[94:95], v221 offset:0
	ds_read_b64 v[96:97], v221 offset:4096
	ds_read_b64 v[98:99], v221 offset:8192
	ds_read_b64 v[100:101], v221 offset:12288
	ds_write2_b32 v215, v146, v147 offset1:16
	ds_write2_b32 v215, v148, v149 offset0:32 offset1:48
	s_waitcnt lgkmcnt(0)
	s_barrier
	ds_read2st64_b32 v[230:231], v216 offset0:32 offset1:48
	ds_read2st64_b32 v[232:233], v216 offset0:40 offset1:56
	v_cmp_gt_u32_e32 vcc, 18, v213
	s_waitcnt vmcnt(0) lgkmcnt(0)
	v_add_f32_e32 v223, v230, v231
	v_add_f32_e32 v224, v232, v233
	v_add_f32_e32 v223, v223, v254
	v_add_f32_e32 v224, v224, v255
	v_max_f32_e32 v223, 0, v223
	v_max_f32_e32 v224, 0, v224
	v_mov_b32_e32 v226, 0xf149f2ca
	v_cndmask_b32_e32 v224, v226, v224, vcc
	v_max_f32_e32 v225, v223, v224
	s_nop 1
	v_max_f32_dpp v226, v225, v225 quad_perm:[1,0,3,2] row_mask:0xf bank_mask:0xf
	s_nop 1
	v_max_f32_dpp v225, v226, v226 quad_perm:[2,3,0,1] row_mask:0xf bank_mask:0xf
	s_nop 1
	v_max_f32_dpp v226, v225, v225 row_half_mirror row_mask:0xf bank_mask:0xf
	s_nop 1
	v_max_f32_dpp v225, v226, v226 row_mirror row_mask:0xf bank_mask:0xf
	ds_swizzle_b32 v226, v225 offset:swizzle(SWAP,16)
	s_waitcnt lgkmcnt(0)
	v_max_f32_e32 v225, v225, v226
	v_sub_f32_e32 v223, v223, v225
	v_sub_f32_e32 v224, v224, v225
	v_mul_f32_e32 v223, 0x3fb8aa3b, v223
	v_mul_f32_e32 v224, 0x3fb8aa3b, v224
	v_exp_f32_e32 v227, v223
	v_exp_f32_e32 v228, v224
	s_nop 0
	v_add_f32_e32 v229, v227, v228
	s_nop 1
	v_add_f32_dpp v226, v229, v229 quad_perm:[1,0,3,2] row_mask:0xf bank_mask:0xf
	s_nop 1
	v_add_f32_dpp v229, v226, v226 quad_perm:[2,3,0,1] row_mask:0xf bank_mask:0xf
	s_nop 1
	v_add_f32_dpp v226, v229, v229 row_half_mirror row_mask:0xf bank_mask:0xf
	s_nop 1
	v_add_f32_dpp v229, v226, v226 row_mirror row_mask:0xf bank_mask:0xf
	ds_swizzle_b32 v226, v229 offset:swizzle(SWAP,16)
	s_waitcnt lgkmcnt(0)
	v_add_f32_e32 v229, v229, v226
	v_rcp_f32_e32 v234, v229
	s_nop 0
	v_mul_f32_e32 v227, v227, v234
	v_mul_f32_e32 v228, v228, v234
	ds_write_b32 v217, v227
	ds_write_b32 v217, v228 offset:128
	s_waitcnt lgkmcnt(0)
	s_barrier
	ds_read_b128 v[102:105], v218 offset:0
	ds_read_b128 v[106:109], v218 offset:16
	ds_read_b128 v[110:113], v218 offset:32
	ds_read_b128 v[114:117], v218 offset:48
	ds_read_b128 v[118:121], v218 offset:64
	ds_read_b128 v[122:125], v218 offset:80
	ds_read_b128 v[126:129], v218 offset:96
	ds_read_b128 v[130:133], v218 offset:112
	ds_read_b128 v[134:137], v218 offset:128
	ds_read_b128 v[138:141], v218 offset:144
	ds_read_b128 v[142:145], v218 offset:160
	ds_read_b128 v[146:149], v218 offset:176
	ds_read_b128 v[150:153], v218 offset:192
	v_mov_b32_e32 v154, 0
	v_mov_b32_e32 v155, 0
	v_mov_b32_e32 v156, 0
	v_mov_b32_e32 v157, 0
	s_waitcnt vmcnt(0) lgkmcnt(0)
	v_fma_mix_f32 v154, v174, v102, v154 op_sel_hi:[1,0,0]
	v_fma_mix_f32 v155, v174, v102, v155 op_sel:[1,0,0] op_sel_hi:[1,0,0]
	v_fma_mix_f32 v156, v175, v102, v156 op_sel_hi:[1,0,0]
	v_fma_mix_f32 v157, v175, v102, v157 op_sel:[1,0,0] op_sel_hi:[1,0,0]
	v_fma_mix_f32 v154, v176, v103, v154 op_sel_hi:[1,0,0]
	v_fma_mix_f32 v155, v176, v103, v155 op_sel:[1,0,0] op_sel_hi:[1,0,0]
	v_fma_mix_f32 v156, v177, v103, v156 op_sel_hi:[1,0,0]
	v_fma_mix_f32 v157, v177, v103, v157 op_sel:[1,0,0] op_sel_hi:[1,0,0]
	v_fma_mix_f32 v154, v178, v104, v154 op_sel_hi:[1,0,0]
	v_fma_mix_f32 v155, v178, v104, v155 op_sel:[1,0,0] op_sel_hi:[1,0,0]
	v_fma_mix_f32 v156, v179, v104, v156 op_sel_hi:[1,0,0]
	v_fma_mix_f32 v157, v179, v104, v157 op_sel:[1,0,0] op_sel_hi:[1,0,0]
	v_fma_mix_f32 v154, v180, v105, v154 op_sel_hi:[1,0,0]
	v_fma_mix_f32 v155, v180, v105, v155 op_sel:[1,0,0] op_sel_hi:[1,0,0]
	v_fma_mix_f32 v156, v181, v105, v156 op_sel_hi:[1,0,0]
	v_fma_mix_f32 v157, v181, v105, v157 op_sel:[1,0,0] op_sel_hi:[1,0,0]
	v_fma_mix_f32 v154, v182, v106, v154 op_sel_hi:[1,0,0]
	v_fma_mix_f32 v155, v182, v106, v155 op_sel:[1,0,0] op_sel_hi:[1,0,0]
	v_fma_mix_f32 v156, v183, v106, v156 op_sel_hi:[1,0,0]
	v_fma_mix_f32 v157, v183, v106, v157 op_sel:[1,0,0] op_sel_hi:[1,0,0]
	v_fma_mix_f32 v154, v184, v107, v154 op_sel_hi:[1,0,0]
	v_fma_mix_f32 v155, v184, v107, v155 op_sel:[1,0,0] op_sel_hi:[1,0,0]
	v_fma_mix_f32 v156, v185, v107, v156 op_sel_hi:[1,0,0]
	v_fma_mix_f32 v157, v185, v107, v157 op_sel:[1,0,0] op_sel_hi:[1,0,0]
	v_fma_mix_f32 v154, v237, v108, v154 op_sel_hi:[1,0,0]
	v_fma_mix_f32 v155, v237, v108, v155 op_sel:[1,0,0] op_sel_hi:[1,0,0]
	v_fma_mix_f32 v156, v238, v108, v156 op_sel_hi:[1,0,0]
	v_fma_mix_f32 v157, v238, v108, v157 op_sel:[1,0,0] op_sel_hi:[1,0,0]
	v_fma_mix_f32 v154, v239, v109, v154 op_sel_hi:[1,0,0]
	v_fma_mix_f32 v155, v239, v109, v155 op_sel:[1,0,0] op_sel_hi:[1,0,0]
	v_fma_mix_f32 v156, v240, v109, v156 op_sel_hi:[1,0,0]
	v_fma_mix_f32 v157, v240, v109, v157 op_sel:[1,0,0] op_sel_hi:[1,0,0]
	v_fma_mix_f32 v154, v241, v110, v154 op_sel_hi:[1,0,0]
	v_fma_mix_f32 v155, v241, v110, v155 op_sel:[1,0,0] op_sel_hi:[1,0,0]
	v_fma_mix_f32 v156, v242, v110, v156 op_sel_hi:[1,0,0]
	v_fma_mix_f32 v157, v242, v110, v157 op_sel:[1,0,0] op_sel_hi:[1,0,0]
	v_fma_mix_f32 v154, v243, v111, v154 op_sel_hi:[1,0,0]
	v_fma_mix_f32 v155, v243, v111, v155 op_sel:[1,0,0] op_sel_hi:[1,0,0]
	v_fma_mix_f32 v156, v244, v111, v156 op_sel_hi:[1,0,0]
	v_fma_mix_f32 v157, v244, v111, v157 op_sel:[1,0,0] op_sel_hi:[1,0,0]
	v_fma_mix_f32 v154, v245, v112, v154 op_sel_hi:[1,0,0]
	v_fma_mix_f32 v155, v245, v112, v155 op_sel:[1,0,0] op_sel_hi:[1,0,0]
	v_fma_mix_f32 v156, v187, v112, v156 op_sel_hi:[1,0,0]
	v_fma_mix_f32 v157, v187, v112, v157 op_sel:[1,0,0] op_sel_hi:[1,0,0]
	v_fma_mix_f32 v154, v188, v113, v154 op_sel_hi:[1,0,0]
	v_fma_mix_f32 v155, v188, v113, v155 op_sel:[1,0,0] op_sel_hi:[1,0,0]
	v_fma_mix_f32 v156, v202, v113, v156 op_sel_hi:[1,0,0]
	v_fma_mix_f32 v157, v202, v113, v157 op_sel:[1,0,0] op_sel_hi:[1,0,0]
	v_fma_mix_f32 v154, v203, v114, v154 op_sel_hi:[1,0,0]
	v_fma_mix_f32 v155, v203, v114, v155 op_sel:[1,0,0] op_sel_hi:[1,0,0]
	v_fma_mix_f32 v156, v204, v114, v156 op_sel_hi:[1,0,0]
	v_fma_mix_f32 v157, v204, v114, v157 op_sel:[1,0,0] op_sel_hi:[1,0,0]
	v_fma_mix_f32 v154, v205, v115, v154 op_sel_hi:[1,0,0]
	v_fma_mix_f32 v155, v205, v115, v155 op_sel:[1,0,0] op_sel_hi:[1,0,0]
	v_fma_mix_f32 v156, v207, v115, v156 op_sel_hi:[1,0,0]
	v_fma_mix_f32 v157, v207, v115, v157 op_sel:[1,0,0] op_sel_hi:[1,0,0]
	v_fma_mix_f32 v154, v30, v116, v154 op_sel_hi:[1,0,0]
	v_fma_mix_f32 v155, v30, v116, v155 op_sel:[1,0,0] op_sel_hi:[1,0,0]
	v_fma_mix_f32 v156, v31, v116, v156 op_sel_hi:[1,0,0]
	v_fma_mix_f32 v157, v31, v116, v157 op_sel:[1,0,0] op_sel_hi:[1,0,0]
	v_fma_mix_f32 v154, v32, v117, v154 op_sel_hi:[1,0,0]
	v_fma_mix_f32 v155, v32, v117, v155 op_sel:[1,0,0] op_sel_hi:[1,0,0]
	v_fma_mix_f32 v156, v33, v117, v156 op_sel_hi:[1,0,0]
	v_fma_mix_f32 v157, v33, v117, v157 op_sel:[1,0,0] op_sel_hi:[1,0,0]
	v_fma_mix_f32 v154, v34, v118, v154 op_sel_hi:[1,0,0]
	v_fma_mix_f32 v155, v34, v118, v155 op_sel:[1,0,0] op_sel_hi:[1,0,0]
	v_fma_mix_f32 v156, v35, v118, v156 op_sel_hi:[1,0,0]
	v_fma_mix_f32 v157, v35, v118, v157 op_sel:[1,0,0] op_sel_hi:[1,0,0]
	v_fma_mix_f32 v154, v36, v119, v154 op_sel_hi:[1,0,0]
	v_fma_mix_f32 v155, v36, v119, v155 op_sel:[1,0,0] op_sel_hi:[1,0,0]
	v_fma_mix_f32 v156, v37, v119, v156 op_sel_hi:[1,0,0]
	v_fma_mix_f32 v157, v37, v119, v157 op_sel:[1,0,0] op_sel_hi:[1,0,0]
	v_fma_mix_f32 v154, v38, v120, v154 op_sel_hi:[1,0,0]
	v_fma_mix_f32 v155, v38, v120, v155 op_sel:[1,0,0] op_sel_hi:[1,0,0]
	v_fma_mix_f32 v156, v39, v120, v156 op_sel_hi:[1,0,0]
	v_fma_mix_f32 v157, v39, v120, v157 op_sel:[1,0,0] op_sel_hi:[1,0,0]
	v_fma_mix_f32 v154, v40, v121, v154 op_sel_hi:[1,0,0]
	v_fma_mix_f32 v155, v40, v121, v155 op_sel:[1,0,0] op_sel_hi:[1,0,0]
	v_fma_mix_f32 v156, v41, v121, v156 op_sel_hi:[1,0,0]
	v_fma_mix_f32 v157, v41, v121, v157 op_sel:[1,0,0] op_sel_hi:[1,0,0]
	v_fma_mix_f32 v154, v42, v122, v154 op_sel_hi:[1,0,0]
	v_fma_mix_f32 v155, v42, v122, v155 op_sel:[1,0,0] op_sel_hi:[1,0,0]
	v_fma_mix_f32 v156, v43, v122, v156 op_sel_hi:[1,0,0]
	v_fma_mix_f32 v157, v43, v122, v157 op_sel:[1,0,0] op_sel_hi:[1,0,0]
	v_fma_mix_f32 v154, v44, v123, v154 op_sel_hi:[1,0,0]
	v_fma_mix_f32 v155, v44, v123, v155 op_sel:[1,0,0] op_sel_hi:[1,0,0]
	v_fma_mix_f32 v156, v45, v123, v156 op_sel_hi:[1,0,0]
	v_fma_mix_f32 v157, v45, v123, v157 op_sel:[1,0,0] op_sel_hi:[1,0,0]
	v_fma_mix_f32 v154, v46, v124, v154 op_sel_hi:[1,0,0]
	v_fma_mix_f32 v155, v46, v124, v155 op_sel:[1,0,0] op_sel_hi:[1,0,0]
	v_fma_mix_f32 v156, v47, v124, v156 op_sel_hi:[1,0,0]
	v_fma_mix_f32 v157, v47, v124, v157 op_sel:[1,0,0] op_sel_hi:[1,0,0]
	v_fma_mix_f32 v154, v48, v125, v154 op_sel_hi:[1,0,0]
	v_fma_mix_f32 v155, v48, v125, v155 op_sel:[1,0,0] op_sel_hi:[1,0,0]
	v_fma_mix_f32 v156, v49, v125, v156 op_sel_hi:[1,0,0]
	v_fma_mix_f32 v157, v49, v125, v157 op_sel:[1,0,0] op_sel_hi:[1,0,0]
	v_fma_mix_f32 v154, v50, v126, v154 op_sel_hi:[1,0,0]
	v_fma_mix_f32 v155, v50, v126, v155 op_sel:[1,0,0] op_sel_hi:[1,0,0]
	v_fma_mix_f32 v156, v51, v126, v156 op_sel_hi:[1,0,0]
	v_fma_mix_f32 v157, v51, v126, v157 op_sel:[1,0,0] op_sel_hi:[1,0,0]
	v_fma_mix_f32 v154, v52, v127, v154 op_sel_hi:[1,0,0]
	v_fma_mix_f32 v155, v52, v127, v155 op_sel:[1,0,0] op_sel_hi:[1,0,0]
	v_fma_mix_f32 v156, v53, v127, v156 op_sel_hi:[1,0,0]
	v_fma_mix_f32 v157, v53, v127, v157 op_sel:[1,0,0] op_sel_hi:[1,0,0]
	v_fma_mix_f32 v154, v54, v128, v154 op_sel_hi:[1,0,0]
	v_fma_mix_f32 v155, v54, v128, v155 op_sel:[1,0,0] op_sel_hi:[1,0,0]
	v_fma_mix_f32 v156, v55, v128, v156 op_sel_hi:[1,0,0]
	v_fma_mix_f32 v157, v55, v128, v157 op_sel:[1,0,0] op_sel_hi:[1,0,0]
	v_fma_mix_f32 v154, v56, v129, v154 op_sel_hi:[1,0,0]
	v_fma_mix_f32 v155, v56, v129, v155 op_sel:[1,0,0] op_sel_hi:[1,0,0]
	v_fma_mix_f32 v156, v57, v129, v156 op_sel_hi:[1,0,0]
	v_fma_mix_f32 v157, v57, v129, v157 op_sel:[1,0,0] op_sel_hi:[1,0,0]
	v_fma_mix_f32 v154, v58, v130, v154 op_sel_hi:[1,0,0]
	v_fma_mix_f32 v155, v58, v130, v155 op_sel:[1,0,0] op_sel_hi:[1,0,0]
	v_fma_mix_f32 v156, v59, v130, v156 op_sel_hi:[1,0,0]
	v_fma_mix_f32 v157, v59, v130, v157 op_sel:[1,0,0] op_sel_hi:[1,0,0]
	v_fma_mix_f32 v154, v60, v131, v154 op_sel_hi:[1,0,0]
	v_fma_mix_f32 v155, v60, v131, v155 op_sel:[1,0,0] op_sel_hi:[1,0,0]
	v_fma_mix_f32 v156, v61, v131, v156 op_sel_hi:[1,0,0]
	v_fma_mix_f32 v157, v61, v131, v157 op_sel:[1,0,0] op_sel_hi:[1,0,0]
	v_fma_mix_f32 v154, v62, v132, v154 op_sel_hi:[1,0,0]
	v_fma_mix_f32 v155, v62, v132, v155 op_sel:[1,0,0] op_sel_hi:[1,0,0]
	v_fma_mix_f32 v156, v63, v132, v156 op_sel_hi:[1,0,0]
	v_fma_mix_f32 v157, v63, v132, v157 op_sel:[1,0,0] op_sel_hi:[1,0,0]
	v_fma_mix_f32 v154, v64, v133, v154 op_sel_hi:[1,0,0]
	v_fma_mix_f32 v155, v64, v133, v155 op_sel:[1,0,0] op_sel_hi:[1,0,0]
	v_fma_mix_f32 v156, v65, v133, v156 op_sel_hi:[1,0,0]
	v_fma_mix_f32 v157, v65, v133, v157 op_sel:[1,0,0] op_sel_hi:[1,0,0]
	v_fma_mix_f32 v154, v66, v134, v154 op_sel_hi:[1,0,0]
	v_fma_mix_f32 v155, v66, v134, v155 op_sel:[1,0,0] op_sel_hi:[1,0,0]
	v_fma_mix_f32 v156, v67, v134, v156 op_sel_hi:[1,0,0]
	v_fma_mix_f32 v157, v67, v134, v157 op_sel:[1,0,0] op_sel_hi:[1,0,0]
	v_fma_mix_f32 v154, v68, v135, v154 op_sel_hi:[1,0,0]
	v_fma_mix_f32 v155, v68, v135, v155 op_sel:[1,0,0] op_sel_hi:[1,0,0]
	v_fma_mix_f32 v156, v69, v135, v156 op_sel_hi:[1,0,0]
	v_fma_mix_f32 v157, v69, v135, v157 op_sel:[1,0,0] op_sel_hi:[1,0,0]
	v_fma_mix_f32 v154, v70, v136, v154 op_sel_hi:[1,0,0]
	v_fma_mix_f32 v155, v70, v136, v155 op_sel:[1,0,0] op_sel_hi:[1,0,0]
	v_fma_mix_f32 v156, v71, v136, v156 op_sel_hi:[1,0,0]
	v_fma_mix_f32 v157, v71, v136, v157 op_sel:[1,0,0] op_sel_hi:[1,0,0]
	v_fma_mix_f32 v154, v72, v137, v154 op_sel_hi:[1,0,0]
	v_fma_mix_f32 v155, v72, v137, v155 op_sel:[1,0,0] op_sel_hi:[1,0,0]
	v_fma_mix_f32 v156, v73, v137, v156 op_sel_hi:[1,0,0]
	v_fma_mix_f32 v157, v73, v137, v157 op_sel:[1,0,0] op_sel_hi:[1,0,0]
	v_fma_mix_f32 v154, v74, v138, v154 op_sel_hi:[1,0,0]
	v_fma_mix_f32 v155, v74, v138, v155 op_sel:[1,0,0] op_sel_hi:[1,0,0]
	v_fma_mix_f32 v156, v75, v138, v156 op_sel_hi:[1,0,0]
	v_fma_mix_f32 v157, v75, v138, v157 op_sel:[1,0,0] op_sel_hi:[1,0,0]
	v_fma_mix_f32 v154, v76, v139, v154 op_sel_hi:[1,0,0]
	v_fma_mix_f32 v155, v76, v139, v155 op_sel:[1,0,0] op_sel_hi:[1,0,0]
	v_fma_mix_f32 v156, v77, v139, v156 op_sel_hi:[1,0,0]
	v_fma_mix_f32 v157, v77, v139, v157 op_sel:[1,0,0] op_sel_hi:[1,0,0]
	v_fma_mix_f32 v154, v78, v140, v154 op_sel_hi:[1,0,0]
	v_fma_mix_f32 v155, v78, v140, v155 op_sel:[1,0,0] op_sel_hi:[1,0,0]
	v_fma_mix_f32 v156, v79, v140, v156 op_sel_hi:[1,0,0]
	v_fma_mix_f32 v157, v79, v140, v157 op_sel:[1,0,0] op_sel_hi:[1,0,0]
	v_fma_mix_f32 v154, v80, v141, v154 op_sel_hi:[1,0,0]
	v_fma_mix_f32 v155, v80, v141, v155 op_sel:[1,0,0] op_sel_hi:[1,0,0]
	v_fma_mix_f32 v156, v81, v141, v156 op_sel_hi:[1,0,0]
	v_fma_mix_f32 v157, v81, v141, v157 op_sel:[1,0,0] op_sel_hi:[1,0,0]
	v_fma_mix_f32 v154, v82, v142, v154 op_sel_hi:[1,0,0]
	v_fma_mix_f32 v155, v82, v142, v155 op_sel:[1,0,0] op_sel_hi:[1,0,0]
	v_fma_mix_f32 v156, v83, v142, v156 op_sel_hi:[1,0,0]
	v_fma_mix_f32 v157, v83, v142, v157 op_sel:[1,0,0] op_sel_hi:[1,0,0]
	v_fma_mix_f32 v154, v84, v143, v154 op_sel_hi:[1,0,0]
	v_fma_mix_f32 v155, v84, v143, v155 op_sel:[1,0,0] op_sel_hi:[1,0,0]
	v_fma_mix_f32 v156, v85, v143, v156 op_sel_hi:[1,0,0]
	v_fma_mix_f32 v157, v85, v143, v157 op_sel:[1,0,0] op_sel_hi:[1,0,0]
	v_fma_mix_f32 v154, v86, v144, v154 op_sel_hi:[1,0,0]
	v_fma_mix_f32 v155, v86, v144, v155 op_sel:[1,0,0] op_sel_hi:[1,0,0]
	v_fma_mix_f32 v156, v87, v144, v156 op_sel_hi:[1,0,0]
	v_fma_mix_f32 v157, v87, v144, v157 op_sel:[1,0,0] op_sel_hi:[1,0,0]
	v_fma_mix_f32 v154, v88, v145, v154 op_sel_hi:[1,0,0]
	v_fma_mix_f32 v155, v88, v145, v155 op_sel:[1,0,0] op_sel_hi:[1,0,0]
	v_fma_mix_f32 v156, v89, v145, v156 op_sel_hi:[1,0,0]
	v_fma_mix_f32 v157, v89, v145, v157 op_sel:[1,0,0] op_sel_hi:[1,0,0]
	v_fma_mix_f32 v154, v90, v146, v154 op_sel_hi:[1,0,0]
	v_fma_mix_f32 v155, v90, v146, v155 op_sel:[1,0,0] op_sel_hi:[1,0,0]
	v_fma_mix_f32 v156, v91, v146, v156 op_sel_hi:[1,0,0]
	v_fma_mix_f32 v157, v91, v146, v157 op_sel:[1,0,0] op_sel_hi:[1,0,0]
	v_fma_mix_f32 v154, v92, v147, v154 op_sel_hi:[1,0,0]
	v_fma_mix_f32 v155, v92, v147, v155 op_sel:[1,0,0] op_sel_hi:[1,0,0]
	v_fma_mix_f32 v156, v93, v147, v156 op_sel_hi:[1,0,0]
	v_fma_mix_f32 v157, v93, v147, v157 op_sel:[1,0,0] op_sel_hi:[1,0,0]
	v_fma_mix_f32 v154, v94, v148, v154 op_sel_hi:[1,0,0]
	v_fma_mix_f32 v155, v94, v148, v155 op_sel:[1,0,0] op_sel_hi:[1,0,0]
	v_fma_mix_f32 v156, v95, v148, v156 op_sel_hi:[1,0,0]
	v_fma_mix_f32 v157, v95, v148, v157 op_sel:[1,0,0] op_sel_hi:[1,0,0]
	v_fma_mix_f32 v154, v96, v149, v154 op_sel_hi:[1,0,0]
	v_fma_mix_f32 v155, v96, v149, v155 op_sel:[1,0,0] op_sel_hi:[1,0,0]
	v_fma_mix_f32 v156, v97, v149, v156 op_sel_hi:[1,0,0]
	v_fma_mix_f32 v157, v97, v149, v157 op_sel:[1,0,0] op_sel_hi:[1,0,0]
	v_fma_mix_f32 v154, v98, v150, v154 op_sel_hi:[1,0,0]
	v_fma_mix_f32 v155, v98, v150, v155 op_sel:[1,0,0] op_sel_hi:[1,0,0]
	v_fma_mix_f32 v156, v99, v150, v156 op_sel_hi:[1,0,0]
	v_fma_mix_f32 v157, v99, v150, v157 op_sel:[1,0,0] op_sel_hi:[1,0,0]
	v_fma_mix_f32 v154, v100, v151, v154 op_sel_hi:[1,0,0]
	v_fma_mix_f32 v155, v100, v151, v155 op_sel:[1,0,0] op_sel_hi:[1,0,0]
	v_fma_mix_f32 v156, v101, v151, v156 op_sel_hi:[1,0,0]
	v_fma_mix_f32 v157, v101, v151, v157 op_sel:[1,0,0] op_sel_hi:[1,0,0]
	global_store_dwordx4 v222, v[154:157], s[8:9]
	s_endpgm
